# baseline (speedup 1.0000x reference)
.LBB1_4:
	s_or_b64 exec, exec, s[12:13]
	v_lshl_or_b32 v8, s2, 3, v8
	v_mov_b32_e32 v151, 0
	v_readfirstlane_b32 s4, v8
	s_ashr_i32 s5, s4, 31
	s_lshl_b64 s[4:5], s[4:5], 2
	s_add_u32 s8, s8, s4
	v_add_u32_e32 v172, 0x22c00, v2
	s_addc_u32 s9, s9, s5
	v_lshl_add_u32 v173, v1, 2, v172
	s_add_u32 s4, s10, s4
	ds_write_b32 v173, v151
	s_addc_u32 s5, s11, s5
	s_load_dword s12, s[6:7], 0x4000
	v_mov_b32_e32 v2, 1
	s_load_dword s8, s[8:9], 0x0
	v_lshrrev_b32_e32 v18, 5, v1
	s_load_dword s3, s[4:5], 0x0
	s_waitcnt lgkmcnt(0)
	s_movk_i32 s4, 0xff
	v_cmp_lt_u32_e32 vcc, s4, v0
	v_bfe_u32 v64, v0, 6, 1
	v_lshlrev_b32_e32 v174, 4, v18
	s_waitcnt vmcnt(12)
	v_lshl_add_u32 v3, v20, 2, v172
	v_lshl_add_u32 v4, v21, 2, v172
	v_lshl_add_u32 v5, v22, 2, v172
	v_lshl_add_u32 v6, v23, 2, v172
	ds_add_u32 v3, v2
	ds_add_u32 v4, v2
	ds_add_u32 v5, v2
	ds_add_u32 v6, v2
	s_waitcnt lgkmcnt(0)
	ds_read_b32 v151, v173
	s_waitcnt lgkmcnt(0)
	v_lshl_or_b32 v2, s8, 6, v1
	v_ashrrev_i32_e32 v3, 31, v2
	v_lshl_add_u64 v[2:3], v[2:3], 2, s[6:7]
	v_cvt_f32_i32_e32 v4, v151
	ds_write_b32 v173, v4 offset:256
	s_waitcnt vmcnt(7)
	s_waitcnt lgkmcnt(0)
	s_barrier
	global_load_dword v175, v[2:3], off
	v_readfirstlane_b32 s18, v0
	s_lshr_b32 s18, s18, 6
	s_and_b32 s19, s18, 1
	s_bfe_u32 s20, s18, 0x10001
	s_lshr_b32 s21, s18, 2
	s_lshl_b32 s22, s19, 12
	s_lshl_b32 s23, s20, 12
	s_lshl_b32 s24, s21, 12
	s_lshl_b32 s25, s19, 7
	v_add_u32_e32 v100, s22, v150
	v_add_u32_e32 v101, s23, v150
	v_add_u32_e32 v102, s24, v150
	v_add_u32_e32 v103, s25, v174
	ds_read_b128 v[2:5], v103 offset:35072
	ds_read_b128 v[6:9], v103 offset:35104
	ds_read_b128 v[10:13], v103 offset:35136
	ds_read_b128 v[14:17], v103 offset:35168
	ds_read_b128 v[34:37], v100 offset:8192
	ds_read_b128 v[38:41], v101
	ds_read_b128 v[18:21], v103 offset:35328
	ds_read_b128 v[22:25], v103 offset:35360
	ds_read_b128 v[26:29], v103 offset:35392
	ds_read_b128 v[30:33], v103 offset:35424
	ds_read_b128 v[42:45], v100 offset:16384
	ds_read_b128 v[46:49], v102
	ds_read_b128 v[50:53], v100 offset:9216
	ds_read_b128 v[54:57], v101 offset:1024
	ds_read_b128 v[58:61], v100 offset:17408
	s_lshl_b32 s27, s19, 14
	s_lshl_b32 s29, s20, 13
	s_or_b32 s27, s27, s29
	s_or_b32 s27, s27, s24
	s_lshl_b32 s28, s21, 11
	s_add_u32 s28, s28, s22
	s_xor_b32 s30, s18, 4
	s_lshl_b32 s30, s30, 10
	s_add_u32 s30, s30, 0x22e00
	s_mov_b32 s26, 0x3e8293ee
	v_add_u32_e32 v76, s27, v213
	v_add_u32_e32 v99, s28, v213
	v_lshl_add_u32 v75, v1, 2, s30
	s_waitcnt lgkmcnt(9)
	v_mfma_f32_32x32x16_bf16 v[2:17], v[34:37], v[38:41], v[2:17]
	ds_read_b128 v[62:65], v102 offset:1024
	s_waitcnt lgkmcnt(4)
	v_mfma_f32_32x32x16_bf16 v[18:33], v[42:45], v[46:49], v[18:33]
	ds_read_b128 v[66:69], v100 offset:10240
	ds_read_b128 v[70:73], v101 offset:2048
	ds_read_b128 v[74:77], v100 offset:18432
	ds_read_b128 v[78:81], v102 offset:2048
	s_waitcnt lgkmcnt(6)
	v_mfma_f32_32x32x16_bf16 v[2:17], v[50:53], v[54:57], v[2:17]
	s_waitcnt lgkmcnt(4)
	v_mfma_f32_32x32x16_bf16 v[18:33], v[58:61], v[62:65], v[18:33]
	ds_read_b128 v[82:85], v100 offset:11264
	ds_read_b128 v[86:89], v101 offset:3072
	ds_read_b128 v[90:93], v100 offset:19456
	ds_read_b128 v[94:97], v102 offset:3072
	s_waitcnt lgkmcnt(6)
	v_mfma_f32_32x32x16_bf16 v[2:17], v[66:69], v[70:73], v[2:17]
	s_waitcnt lgkmcnt(4)
	v_mfma_f32_32x32x16_bf16 v[18:33], v[74:77], v[78:81], v[18:33]
	s_cmp_eq_u32 s20, 1
	s_cbranch_scc0 .Levt_nov1
	v_and_b32_e32 v98, 31, v1
	v_lshlrev_b32_e32 v98, 2, v98
	v_add_u32_e32 v98, s25, v98
	ds_read_b32 v104, v98 offset:35584
	ds_read_b128 v[120:123], v100 offset:24576
	ds_read_b128 v[124:127], v100 offset:25600
	ds_read_b128 v[128:131], v100 offset:26624
	ds_read_b128 v[132:135], v100 offset:27648
	s_waitcnt lgkmcnt(4)
	v_mov_b32_e32 v105, v104
	v_mov_b32_e32 v106, v104
	v_mov_b32_e32 v107, v104
	v_mov_b32_e32 v108, v104
	v_mov_b32_e32 v109, v104
	v_mov_b32_e32 v110, v104
	v_mov_b32_e32 v111, v104
	v_mov_b32_e32 v112, v104
	v_mov_b32_e32 v113, v104
	v_mov_b32_e32 v114, v104
	v_mov_b32_e32 v115, v104
	v_mov_b32_e32 v116, v104
	v_mov_b32_e32 v117, v104
	v_mov_b32_e32 v118, v104
	v_mov_b32_e32 v119, v104
	s_waitcnt lgkmcnt(0)
	s_nop 1
	v_mfma_f32_32x32x16_bf16 v[104:119], v[46:49], v[120:123], v[104:119]
	v_mfma_f32_32x32x16_bf16 v[104:119], v[62:65], v[124:127], v[104:119]
	v_mfma_f32_32x32x16_bf16 v[104:119], v[78:81], v[128:131], v[104:119]
	v_mfma_f32_32x32x16_bf16 v[104:119], v[94:97], v[132:135], v[104:119]
.Levt_nov1:
	s_waitcnt lgkmcnt(2)
	v_mfma_f32_32x32x16_bf16 v[2:17], v[82:85], v[86:89], v[2:17]
	s_waitcnt lgkmcnt(0)
	v_mfma_f32_32x32x16_bf16 v[18:33], v[90:93], v[94:97], v[18:33]
	s_nop 10
	v_cvt_pk_bf16_f32 v34, v2, v3
	v_cvt_pk_bf16_f32 v35, v4, v5
	v_cvt_pk_bf16_f32 v36, v6, v7
	v_cvt_pk_bf16_f32 v37, v8, v9
	v_cvt_pk_bf16_f32 v42, v18, v19
	v_cvt_pk_bf16_f32 v43, v20, v21
	v_cvt_pk_bf16_f32 v44, v22, v23
	v_cvt_pk_bf16_f32 v45, v24, v25
	v_cvt_pk_bf16_f32 v38, v10, v11
	v_cvt_pk_bf16_f32 v39, v12, v13
	v_cvt_pk_bf16_f32 v40, v14, v15
	v_cvt_pk_bf16_f32 v41, v16, v17
	v_cvt_pk_bf16_f32 v50, v26, v27
	v_cvt_pk_bf16_f32 v51, v28, v29
	v_cvt_pk_bf16_f32 v52, v30, v31
	v_cvt_pk_bf16_f32 v53, v32, v33
	s_nop 1
	v_mfma_f32_32x32x16_bf16 v[54:69], v[42:45], v[34:37], 0
	v_mfma_f32_32x32x16_bf16 v[54:69], v[50:53], v[38:41], v[54:69]
	s_cmp_eq_u32 s20, 1
	s_cbranch_scc0 .Levt_nov2
	v_cvt_pk_bf16_f32 v120, v104, v105
	v_cvt_pk_bf16_f32 v121, v106, v107
	v_cvt_pk_bf16_f32 v122, v108, v109
	v_cvt_pk_bf16_f32 v123, v110, v111
	v_cvt_pk_bf16_f32 v124, v112, v113
	v_cvt_pk_bf16_f32 v125, v114, v115
	v_cvt_pk_bf16_f32 v126, v116, v117
	v_cvt_pk_bf16_f32 v127, v118, v119
	ds_write_b128 v99, v[120:123] offset:32768
	ds_write_b128 v99, v[124:127] offset:33792
	s_branch .Levt_join2
.Levt_nov2:
	s_nop 11
.Levt_join2:
	s_nop 1
	v_mul_f32_e32 v54, s26, v54
	v_mul_f32_e32 v55, s26, v55
	v_mul_f32_e32 v56, s26, v56
	v_mul_f32_e32 v57, s26, v57
	v_mul_f32_e32 v58, s26, v58
	v_mul_f32_e32 v59, s26, v59
	v_mul_f32_e32 v60, s26, v60
	v_mul_f32_e32 v61, s26, v61
	v_mul_f32_e32 v62, s26, v62
	v_mul_f32_e32 v63, s26, v63
	v_mul_f32_e32 v64, s26, v64
	v_mul_f32_e32 v65, s26, v65
	v_mul_f32_e32 v66, s26, v66
	v_mul_f32_e32 v67, s26, v67
	v_mul_f32_e32 v68, s26, v68
	v_mul_f32_e32 v69, s26, v69
	v_max3_f32 v70, v54, v55, v56
	v_max3_f32 v71, v57, v58, v59
	v_max3_f32 v72, v60, v61, v62
	v_max3_f32 v73, v63, v64, v65
	v_max3_f32 v74, v66, v67, v68
	v_max3_f32 v70, v70, v71, v72
	v_max3_f32 v73, v73, v74, v69
	v_max_f32_e32 v70, v70, v73
	v_mov_b32_e32 v71, v70
	s_nop 1
	v_permlane32_swap_b32_e32 v70, v71
	v_max_f32_e32 v70, v70, v71
	ds_write_b32 v173, v70 offset:512
	s_waitcnt lgkmcnt(0)
	s_barrier
	ds_read_b32 v71, v75
	s_waitcnt lgkmcnt(0)
	v_max_f32_e32 v70, v70, v71
	v_sub_f32_e32 v54, v54, v70
	v_sub_f32_e32 v55, v55, v70
	v_sub_f32_e32 v56, v56, v70
	v_sub_f32_e32 v57, v57, v70
	v_sub_f32_e32 v58, v58, v70
	v_sub_f32_e32 v59, v59, v70
	v_sub_f32_e32 v60, v60, v70
	v_sub_f32_e32 v61, v61, v70
	v_sub_f32_e32 v62, v62, v70
	v_sub_f32_e32 v63, v63, v70
	v_sub_f32_e32 v64, v64, v70
	v_sub_f32_e32 v65, v65, v70
	v_sub_f32_e32 v66, v66, v70
	v_sub_f32_e32 v67, v67, v70
	v_sub_f32_e32 v68, v68, v70
	v_sub_f32_e32 v69, v69, v70
	v_exp_f32_e32 v54, v54
	v_exp_f32_e32 v55, v55
	v_exp_f32_e32 v56, v56
	v_exp_f32_e32 v57, v57
	s_nop 0
	ds_write_b128 v76, v[54:57]
	v_exp_f32_e32 v58, v58
	v_exp_f32_e32 v59, v59
	v_exp_f32_e32 v60, v60
	v_exp_f32_e32 v61, v61
	s_nop 0
	ds_write_b128 v76, v[58:61] offset:1024
	v_exp_f32_e32 v62, v62
	v_exp_f32_e32 v63, v63
	v_exp_f32_e32 v64, v64
	v_exp_f32_e32 v65, v65
	s_nop 0
	ds_write_b128 v76, v[62:65] offset:2048
	v_exp_f32_e32 v66, v66
	v_exp_f32_e32 v67, v67
	v_exp_f32_e32 v68, v68
	v_exp_f32_e32 v69, v69
	s_nop 0
	ds_write_b128 v76, v[66:69] offset:3072
	s_load_dwordx4 s[8:11], s[0:1], 0x48
	v_mov_b32_e32 v2, v174
	v_add_u32_e32 v10, v172, v2
	s_waitcnt vmcnt(1) lgkmcnt(0)
	s_barrier
	ds_read_b128 v[18:21], v10 offset:256
	ds_read_b128 v[22:25], v10 offset:288
	ds_read_b128 v[82:85], v10 offset:320
	ds_read_b128 v[86:89], v10 offset:352
	ds_read_b128 v[74:77], v10 offset:384
	ds_read_b128 v[78:81], v10 offset:416
	ds_read_b128 v[2:5], v213 offset:32768
	ds_read_b128 v[6:9], v213 offset:0
	ds_read_b128 v[66:69], v10 offset:448
	ds_read_b128 v[70:73], v10 offset:480
	ds_read_b128 v[10:13], v213 offset:1024
	s_waitcnt lgkmcnt(3)
	v_pk_mul_f32 v[26:27], v[8:9], v[20:21]
	v_pk_mul_f32 v[28:29], v[6:7], v[18:19]
	ds_read_b128 v[14:17], v213 offset:8192
	s_waitcnt lgkmcnt(1)
	v_pk_mul_f32 v[12:13], v[12:13], v[24:25]
	v_pk_mul_f32 v[10:11], v[10:11], v[22:23]
	v_pk_fma_f32 v[30:31], v[8:9], v[20:21], v[12:13]
	v_pk_fma_f32 v[32:33], v[6:7], v[18:19], v[10:11]
	v_cvt_pk_bf16_f32 v9, v12, v13
	v_cvt_pk_bf16_f32 v7, v26, v27
	v_cvt_pk_bf16_f32 v8, v10, v11
	v_cvt_pk_bf16_f32 v6, v28, v29
	ds_read_b128 v[10:13], v213 offset:33792
	s_nop 0
	v_mfma_f32_32x32x16_bf16 v[34:49], v[2:5], v[6:9], 0
	ds_read_b128 v[6:9], v213 offset:9216
	s_waitcnt lgkmcnt(2)
	v_mul_f32_e32 v26, v16, v20
	v_mul_f32_e32 v27, v17, v21
	v_pk_mul_f32 v[50:51], v[14:15], v[18:19]
	s_mov_b32 s4, 0x3727c5ac
	s_waitcnt lgkmcnt(0)
	v_pk_mul_f32 v[8:9], v[8:9], v[24:25]
	v_pk_mul_f32 v[28:29], v[6:7], v[22:23]
	v_pk_fma_f32 v[90:91], v[16:17], v[20:21], v[8:9]
	v_pk_fma_f32 v[92:93], v[14:15], v[18:19], v[28:29]
	ds_read_b128 v[14:17], v213 offset:2048
	v_cvt_pk_bf16_f32 v9, v8, v9
	v_cvt_pk_bf16_f32 v7, v26, v27
	v_cvt_pk_bf16_f32 v8, v28, v29
	ds_read_b128 v[26:29], v213 offset:3072
	v_cvt_pk_bf16_f32 v6, v50, v51
	s_waitcnt lgkmcnt(1)
	v_pk_mul_f32 v[94:95], v[14:15], v[82:83]
	s_mov_b32 s0, 0x3c800000
	v_mfma_f32_32x32x16_bf16 v[50:65], v[2:5], v[6:9], 0
	v_mul_f32_e32 v2, v16, v84
	v_mul_f32_e32 v3, v17, v85
	s_waitcnt lgkmcnt(0)
	v_mul_f32_e32 v4, v28, v88
	v_mul_f32_e32 v5, v29, v89
	v_pk_mul_f32 v[6:7], v[26:27], v[86:87]
	v_pk_fma_f32 v[8:9], v[16:17], v[84:85], v[4:5]
	v_cvt_pk_bf16_f32 v3, v2, v3
	v_pk_fma_f32 v[14:15], v[14:15], v[82:83], v[6:7]
	v_pk_add_f32 v[26:27], v[8:9], v[30:31]
	v_cvt_pk_bf16_f32 v5, v4, v5
	v_cvt_pk_bf16_f32 v4, v6, v7
	ds_read_b128 v[6:9], v213 offset:10240
	v_pk_add_f32 v[28:29], v[14:15], v[32:33]
	ds_read_b128 v[14:17], v213 offset:11264
	v_cvt_pk_bf16_f32 v2, v94, v95
	s_waitcnt lgkmcnt(1)
	v_pk_mul_f32 v[30:31], v[6:7], v[82:83]
	v_mov_b64_e32 v[152:153], s[4:5]
	v_mfma_f32_32x32x16_bf16 v[34:49], v[10:13], v[2:5], v[34:49]
	v_mul_f32_e32 v2, v8, v84
	v_mul_f32_e32 v3, v9, v85
	s_waitcnt lgkmcnt(0)
	v_mul_f32_e32 v4, v16, v88
	v_mul_f32_e32 v5, v17, v89
	v_pk_mul_f32 v[14:15], v[14:15], v[86:87]
	v_pk_fma_f32 v[8:9], v[8:9], v[84:85], v[4:5]
	v_pk_fma_f32 v[6:7], v[6:7], v[82:83], v[14:15]
	v_cvt_pk_bf16_f32 v5, v4, v5
	v_cvt_pk_bf16_f32 v3, v2, v3
	v_cvt_pk_bf16_f32 v4, v14, v15
	v_pk_add_f32 v[32:33], v[8:9], v[90:91]
	v_pk_add_f32 v[90:91], v[6:7], v[92:93]
	ds_read_b128 v[6:9], v213 offset:34816
	ds_read_b128 v[14:17], v213 offset:4096
	v_cvt_pk_bf16_f32 v2, v30, v31
	s_mov_b32 s13, 0
	s_mov_b64 s[6:7], 0
	v_mfma_f32_32x32x16_bf16 v[50:65], v[10:13], v[2:5], v[50:65]
	ds_read_b128 v[2:5], v213 offset:5120
	ds_read_b128 v[10:13], v213 offset:12288
	s_waitcnt lgkmcnt(2)
	v_pk_mul_f32 v[30:31], v[16:17], v[76:77]
	v_pk_mul_f32 v[92:93], v[14:15], v[74:75]
	s_waitcnt lgkmcnt(1)
	v_pk_mul_f32 v[4:5], v[4:5], v[80:81]
	v_pk_mul_f32 v[94:95], v[2:3], v[78:79]
	v_pk_fma_f32 v[2:3], v[16:17], v[76:77], v[4:5]
	v_cvt_pk_bf16_f32 v5, v4, v5
	v_pk_add_f32 v[96:97], v[2:3], v[26:27]
	v_cvt_pk_bf16_f32 v3, v30, v31
	v_cvt_pk_bf16_f32 v4, v94, v95
	v_cvt_pk_bf16_f32 v2, v92, v93
	v_pk_fma_f32 v[14:15], v[14:15], v[74:75], v[94:95]
	s_waitcnt lgkmcnt(0)
	v_pk_mul_f32 v[30:31], v[10:11], v[74:75]
	v_mfma_f32_32x32x16_bf16 v[34:49], v[6:9], v[2:5], v[34:49]
	ds_read_b128 v[2:5], v213 offset:13312
	v_add_f32_e32 v98, v14, v28
	v_add_f32_e32 v99, v15, v29
	ds_read_b128 v[14:17], v213 offset:35840
	v_pk_mul_f32 v[26:27], v[12:13], v[76:77]
	s_waitcnt lgkmcnt(1)
	v_pk_mul_f32 v[4:5], v[4:5], v[80:81]
	v_pk_mul_f32 v[28:29], v[2:3], v[78:79]
	v_pk_fma_f32 v[2:3], v[12:13], v[76:77], v[4:5]
	v_pk_fma_f32 v[10:11], v[10:11], v[74:75], v[28:29]
	v_pk_add_f32 v[32:33], v[2:3], v[32:33]
	v_pk_add_f32 v[92:93], v[10:11], v[90:91]
	ds_read_b128 v[10:13], v213 offset:6144
	v_cvt_pk_bf16_f32 v5, v4, v5
	v_cvt_pk_bf16_f32 v3, v26, v27
	v_cvt_pk_bf16_f32 v4, v28, v29
	ds_read_b128 v[26:29], v213 offset:7168
	v_cvt_pk_bf16_f32 v2, v30, v31
	s_waitcnt lgkmcnt(1)
	v_pk_mul_f32 v[30:31], v[10:11], v[66:67]
	v_mfma_f32_32x32x16_bf16 v[50:65], v[6:9], v[2:5], v[50:65]
	v_mul_f32_e32 v2, v12, v68
	v_mul_f32_e32 v3, v13, v69
	s_waitcnt lgkmcnt(0)
	v_mul_f32_e32 v4, v28, v72
	v_mul_f32_e32 v5, v29, v73
	v_pk_mul_f32 v[6:7], v[26:27], v[70:71]
	v_pk_fma_f32 v[8:9], v[12:13], v[68:69], v[4:5]
	v_cvt_pk_bf16_f32 v3, v2, v3
	v_pk_fma_f32 v[10:11], v[10:11], v[66:67], v[6:7]
	v_pk_add_f32 v[94:95], v[8:9], v[96:97]
	v_cvt_pk_bf16_f32 v5, v4, v5
	v_cvt_pk_bf16_f32 v4, v6, v7
	ds_read_b128 v[6:9], v213 offset:14336
	v_pk_add_f32 v[96:97], v[10:11], v[98:99]
	ds_read_b128 v[10:13], v213 offset:15360
	v_cvt_pk_bf16_f32 v2, v30, v31
	s_waitcnt lgkmcnt(1)
	v_pk_mul_f32 v[30:31], v[6:7], v[66:67]
	v_mfma_f32_32x32x16_bf16 v[34:49], v[14:17], v[2:5], v[34:49]
	s_waitcnt lgkmcnt(0)
	v_mul_f32_e32 v10, v10, v70
	v_mul_f32_e32 v11, v11, v71
	v_mul_f32_e32 v2, v8, v68
	v_mul_f32_e32 v3, v9, v69
	v_pk_mul_f32 v[4:5], v[12:13], v[72:73]
	v_pk_fma_f32 v[6:7], v[6:7], v[66:67], v[10:11]
	v_pk_fma_f32 v[8:9], v[8:9], v[68:69], v[4:5]
	v_pk_add_f32 v[92:93], v[6:7], v[92:93]
	v_cvt_pk_bf16_f32 v3, v2, v3
	v_pk_add_f32 v[90:91], v[8:9], v[32:33]
	v_cvt_pk_bf16_f32 v5, v4, v5
	v_cvt_pk_bf16_f32 v4, v10, v11
	ds_read_b128 v[26:29], v213 offset:36864
	ds_read_b128 v[6:9], v213 offset:16384
	v_cvt_pk_bf16_f32 v2, v30, v31
	ds_read_b128 v[98:101], v213 offset:25600
	ds_read_b128 v[102:105], v213 offset:37888
	v_mfma_f32_32x32x16_bf16 v[50:65], v[14:17], v[2:5], v[50:65]
	ds_read_b128 v[2:5], v213 offset:17408
	ds_read_b128 v[30:33], v213 offset:24576
	s_waitcnt lgkmcnt(4)
	v_pk_mul_f32 v[12:13], v[6:7], v[18:19]
	v_pk_mul_f32 v[10:11], v[8:9], v[20:21]
	s_waitcnt lgkmcnt(1)
	v_pk_mul_f32 v[14:15], v[2:3], v[22:23]
	v_pk_mul_f32 v[22:23], v[98:99], v[22:23]
	v_pk_fma_f32 v[112:113], v[6:7], v[18:19], v[14:15]
	s_waitcnt lgkmcnt(0)
	v_pk_mul_f32 v[114:115], v[30:31], v[18:19]
	v_pk_fma_f32 v[118:119], v[30:31], v[18:19], v[22:23]
	v_pk_mul_f32 v[4:5], v[4:5], v[24:25]
	v_pk_mul_f32 v[106:107], v[32:33], v[20:21]
	v_pk_mul_f32 v[24:25], v[100:101], v[24:25]
	ds_read_b128 v[98:101], v213 offset:18432
	v_cvt_pk_bf16_f32 v19, v106, v107
	ds_read_b128 v[106:109], v213 offset:19456
	v_pk_fma_f32 v[110:111], v[8:9], v[20:21], v[4:5]
	v_cvt_pk_bf16_f32 v5, v4, v5
	v_cvt_pk_bf16_f32 v3, v10, v11
	v_cvt_pk_bf16_f32 v4, v14, v15
	s_waitcnt lgkmcnt(0)
	v_pk_mul_f32 v[106:107], v[106:107], v[86:87]
	v_cvt_pk_bf16_f32 v2, v12, v13
	v_pk_mul_f32 v[120:121], v[98:99], v[82:83]
	v_pk_mul_f32 v[108:109], v[108:109], v[88:89]
	v_pk_fma_f32 v[98:99], v[98:99], v[82:83], v[106:107]
	v_mfma_f32_32x32x16_bf16 v[2:17], v[26:29], v[2:5], 0
	v_cvt_pk_bf16_f32 v18, v114, v115
	v_mul_f32_e32 v114, v100, v84
	v_mul_f32_e32 v115, v101, v85
	v_fma_f32 v100, v100, v84, v108
	v_fma_f32 v101, v101, v85, v109
	v_pk_add_f32 v[124:125], v[98:99], v[112:113]
	v_pk_add_f32 v[122:123], v[100:101], v[110:111]
	v_cvt_pk_bf16_f32 v101, v108, v109
	v_cvt_pk_bf16_f32 v100, v106, v107
	ds_read_b128 v[106:109], v213 offset:26624
	v_pk_fma_f32 v[116:117], v[32:33], v[20:21], v[24:25]
	v_cvt_pk_bf16_f32 v21, v24, v25
	v_cvt_pk_bf16_f32 v20, v22, v23
	ds_read_b128 v[110:113], v213 offset:27648
	v_cvt_pk_bf16_f32 v99, v114, v115
	v_mfma_f32_32x32x16_bf16 v[18:33], v[26:29], v[18:21], 0
	v_cvt_pk_bf16_f32 v98, v120, v121
	s_waitcnt lgkmcnt(1)
	v_mul_f32_e32 v114, v106, v82
	v_mul_f32_e32 v115, v107, v83
	s_waitcnt lgkmcnt(0)
	v_pk_mul_f32 v[86:87], v[110:111], v[86:87]
	v_pk_mul_f32 v[88:89], v[112:113], v[88:89]
	v_pk_fma_f32 v[82:83], v[106:107], v[82:83], v[86:87]
	v_mfma_f32_32x32x16_bf16 v[2:17], v[102:105], v[98:101], v[2:17]
	v_mul_f32_e32 v98, v108, v84
	v_mul_f32_e32 v99, v109, v85
	v_fma_f32 v84, v108, v84, v88
	v_fma_f32 v85, v109, v85, v89
	v_add_f32_e32 v108, v82, v118
	v_add_f32_e32 v109, v83, v119
	v_cvt_pk_bf16_f32 v83, v98, v99
	v_pk_add_f32 v[106:107], v[84:85], v[116:117]
	v_cvt_pk_bf16_f32 v85, v88, v89
	v_cvt_pk_bf16_f32 v84, v86, v87
	ds_read_b128 v[86:89], v213 offset:38912
	ds_read_b128 v[98:101], v213 offset:20480
	v_cvt_pk_bf16_f32 v82, v114, v115
	s_waitcnt lgkmcnt(0)
	v_pk_mul_f32 v[110:111], v[100:101], v[76:77]
	v_mfma_f32_32x32x16_bf16 v[18:33], v[102:105], v[82:85], v[18:33]
	ds_read_b128 v[82:85], v213 offset:21504
	ds_read_b128 v[102:105], v213 offset:28672
	v_mul_f32_e32 v112, v98, v74
	v_mul_f32_e32 v113, v99, v75
	s_waitcnt lgkmcnt(1)
	v_pk_mul_f32 v[84:85], v[84:85], v[80:81]
	v_pk_mul_f32 v[114:115], v[82:83], v[78:79]
	v_pk_fma_f32 v[82:83], v[100:101], v[76:77], v[84:85]
	v_cvt_pk_bf16_f32 v85, v84, v85
	v_pk_add_f32 v[116:117], v[82:83], v[122:123]
	v_cvt_pk_bf16_f32 v83, v110, v111
	v_cvt_pk_bf16_f32 v84, v114, v115
	v_cvt_pk_bf16_f32 v82, v112, v113
	v_pk_fma_f32 v[98:99], v[98:99], v[74:75], v[114:115]
	s_waitcnt lgkmcnt(0)
	v_pk_mul_f32 v[112:113], v[102:103], v[74:75]
	v_mfma_f32_32x32x16_bf16 v[2:17], v[86:89], v[82:85], v[2:17]
	ds_read_b128 v[82:85], v213 offset:29696
	v_add_f32_e32 v118, v98, v124
	v_add_f32_e32 v119, v99, v125
	v_mul_f32_e32 v110, v104, v76
	v_mul_f32_e32 v111, v105, v77
	ds_read_b128 v[98:101], v213 offset:39936
	s_waitcnt lgkmcnt(1)
	v_pk_mul_f32 v[78:79], v[82:83], v[78:79]
	v_pk_mul_f32 v[80:81], v[84:85], v[80:81]
	v_pk_fma_f32 v[74:75], v[102:103], v[74:75], v[78:79]
	v_pk_fma_f32 v[76:77], v[104:105], v[76:77], v[80:81]
	v_pk_add_f32 v[104:105], v[74:75], v[108:109]
	v_pk_add_f32 v[102:103], v[76:77], v[106:107]
	v_cvt_pk_bf16_f32 v77, v80, v81
	v_cvt_pk_bf16_f32 v76, v78, v79
	ds_read_b128 v[78:81], v213 offset:22528
	ds_read_b128 v[82:85], v213 offset:23552
	v_cvt_pk_bf16_f32 v75, v110, v111
	v_cvt_pk_bf16_f32 v74, v112, v113
	s_waitcnt lgkmcnt(0)
	v_pk_mul_f32 v[82:83], v[82:83], v[70:71]
	v_mfma_f32_32x32x16_bf16 v[18:33], v[86:89], v[74:77], v[18:33]
	v_mul_f32_e32 v74, v80, v68
	v_mul_f32_e32 v75, v81, v69
	v_mul_f32_e32 v76, v84, v72
	v_mul_f32_e32 v77, v85, v73
	v_mul_f32_e32 v86, v78, v66
	v_mul_f32_e32 v87, v79, v67
	v_pk_fma_f32 v[80:81], v[80:81], v[68:69], v[76:77]
	v_pk_fma_f32 v[78:79], v[78:79], v[66:67], v[82:83]
	v_cvt_pk_bf16_f32 v75, v74, v75
	v_pk_add_f32 v[88:89], v[80:81], v[116:117]
	v_pk_add_f32 v[106:107], v[78:79], v[118:119]
	ds_read_b128 v[78:81], v213 offset:30720
	v_cvt_pk_bf16_f32 v77, v76, v77
	v_cvt_pk_bf16_f32 v76, v82, v83
	ds_read_b128 v[82:85], v213 offset:31744
	v_cvt_pk_bf16_f32 v74, v86, v87
	s_waitcnt lgkmcnt(0)
	v_pk_mul_f32 v[72:73], v[84:85], v[72:73]
	v_mfma_f32_32x32x16_bf16 v[2:17], v[98:101], v[74:77], v[2:17]
	v_mul_f32_e32 v74, v80, v68
	v_mul_f32_e32 v75, v81, v69
	v_fma_f32 v68, v80, v68, v72
	v_fma_f32 v69, v81, v69, v73
	v_mul_f32_e32 v70, v82, v70
	v_mul_f32_e32 v71, v83, v71
	v_pk_add_f32 v[84:85], v[68:69], v[102:103]
	v_cvt_pk_bf16_f32 v69, v72, v73
	v_pk_mov_b32 v[72:73], v[96:97], v[94:95] op_sel:[1,0]
	v_mov_b32_e32 v97, v95
	v_pk_add_f32 v[72:73], v[72:73], v[96:97]
	v_pk_mul_f32 v[76:77], v[78:79], v[66:67]
	v_pk_fma_f32 v[66:67], v[78:79], v[66:67], v[70:71]
	v_pk_add_f32 v[72:73], v[72:73], v[72:73] op_sel:[0,1] op_sel_hi:[1,0]
	v_pk_add_f32 v[86:87], v[66:67], v[104:105]
	v_mov_b32_e32 v66, v72
	s_nop 1
	v_permlane32_swap_b32_e32 v72, v66
	v_add_f32_e32 v66, v72, v66
	v_cvt_pk_bf16_f32 v67, v74, v75
	v_rcp_f32_e32 v74, v66
	v_cvt_pk_bf16_f32 v68, v70, v71
	v_cvt_pk_bf16_f32 v66, v76, v77
	v_pk_mul_f32 v[70:71], v[46:47], v[74:75] op_sel_hi:[1,0]
	s_nop 0
	v_mfma_f32_32x32x16_bf16 v[18:33], v[98:101], v[66:69], v[18:33]
	v_mul_f32_e32 v66, v42, v74
	v_mul_f32_e32 v67, v43, v74
	v_pk_mov_b32 v[42:43], v[92:93], v[90:91] op_sel:[1,0]
	v_mov_b32_e32 v93, v91
	v_pk_add_f32 v[42:43], v[42:43], v[92:93]
	v_pk_mul_f32 v[68:69], v[44:45], v[74:75] op_sel_hi:[1,0]
	v_pk_add_f32 v[42:43], v[42:43], v[42:43] op_sel:[0,1] op_sel_hi:[1,0]
	v_pk_mov_b32 v[44:45], v[106:107], v[88:89] op_sel:[1,0]
	v_mov_b32_e32 v43, v42
	s_nop 1
	v_permlane32_swap_b32_e32 v42, v43
	v_add_f32_e32 v42, v42, v43
	v_rcp_f32_e32 v42, v42
	v_mov_b32_e32 v107, v89
	v_pk_add_f32 v[44:45], v[44:45], v[106:107]
	v_pk_mul_f32 v[72:73], v[48:49], v[74:75] op_sel_hi:[1,0]
	v_pk_add_f32 v[44:45], v[44:45], v[44:45] op_sel:[0,1] op_sel_hi:[1,0]
	v_pk_mul_f32 v[36:37], v[36:37], v[74:75] op_sel_hi:[1,0]
	v_pk_mul_f32 v[38:39], v[38:39], v[74:75] op_sel_hi:[1,0]
	v_pk_mul_f32 v[40:41], v[40:41], v[74:75] op_sel_hi:[1,0]
	v_pk_mul_f32 v[34:35], v[34:35], v[74:75] op_sel_hi:[1,0]
	v_pk_mul_f32 v[74:75], v[58:59], v[42:43] op_sel_hi:[1,0]
	v_pk_mul_f32 v[78:79], v[60:61], v[42:43] op_sel_hi:[1,0]
	v_pk_mul_f32 v[80:81], v[62:63], v[42:43] op_sel_hi:[1,0]
	v_pk_mul_f32 v[82:83], v[64:65], v[42:43] op_sel_hi:[1,0]
	v_pk_mul_f32 v[92:93], v[52:53], v[42:43] op_sel_hi:[1,0]
	v_mov_b32_e32 v43, v44
	s_nop 1
	v_permlane32_swap_b32_e32 v44, v43
	v_add_f32_e32 v43, v44, v43
	v_rcp_f32_e32 v76, v43
	v_pk_mul_f32 v[96:97], v[54:55], v[42:43] op_sel_hi:[1,0]
	v_pk_mul_f32 v[94:95], v[56:57], v[42:43] op_sel_hi:[1,0]
	v_pk_mul_f32 v[98:99], v[50:51], v[42:43] op_sel_hi:[1,0]
	v_pk_mul_f32 v[100:101], v[4:5], v[76:77] op_sel_hi:[1,0]
	v_pk_mov_b32 v[4:5], v[86:87], v[84:85] op_sel:[1,0]
	v_mov_b32_e32 v87, v85
	v_pk_add_f32 v[4:5], v[4:5], v[86:87]
	v_pk_mul_f32 v[102:103], v[6:7], v[76:77] op_sel_hi:[1,0]
	v_pk_add_f32 v[104:105], v[4:5], v[4:5] op_sel:[0,1] op_sel_hi:[1,0]
	v_cvt_pk_bf16_f32 v7, v40, v41
	ds_read_b128 v[84:87], v150 offset:52224
	ds_read_b128 v[50:53], v150 offset:35840
	ds_read_b128 v[54:57], v150 offset:36864
	ds_read_b128 v[58:61], v150 offset:37888
	ds_read_b128 v[62:65], v150 offset:38912
	v_cvt_pk_bf16_f32 v6, v38, v39
	v_cvt_pk_bf16_f32 v5, v36, v37
	v_cvt_pk_bf16_f32 v4, v34, v35
	ds_read_b128 v[88:91], v150 offset:53248
	ds_read_b128 v[34:37], v150 offset:39936
	ds_read_b128 v[38:41], v150 offset:40960
	ds_read_b128 v[42:45], v150 offset:41984
	ds_read_b128 v[46:49], v150 offset:43008
	v_cvt_pk_bf16_f32 v95, v94, v95
	v_cvt_pk_bf16_f32 v94, v96, v97
	v_cvt_pk_bf16_f32 v93, v92, v93
	v_cvt_pk_bf16_f32 v92, v98, v99
	s_waitcnt lgkmcnt(5)
	v_mfma_f32_32x32x16_bf16 v[50:65], v[84:87], v[4:7], v[50:65]
	v_mul_f32_e32 v10, v10, v76
	v_mul_f32_e32 v11, v11, v76
	v_mul_f32_e32 v12, v12, v76
	v_mul_f32_e32 v13, v13, v76
	v_mul_f32_e32 v8, v8, v76
	v_mul_f32_e32 v9, v9, v76
	v_mov_b32_e32 v77, v104
	s_nop 1
	v_permlane32_swap_b32_e32 v104, v77
	v_cvt_pk_bf16_f32 v73, v72, v73
	s_waitcnt lgkmcnt(0)
	v_mfma_f32_32x32x16_bf16 v[34:49], v[84:87], v[92:95], v[34:49]
	v_cvt_pk_bf16_f32 v72, v70, v71
	v_cvt_pk_bf16_f32 v70, v66, v67
	v_add_f32_e32 v66, v104, v77
	v_cvt_pk_bf16_f32 v71, v68, v69
	v_rcp_f32_e32 v104, v66
	v_cvt_pk_bf16_f32 v69, v82, v83
	v_cvt_pk_bf16_f32 v68, v80, v81
	v_cvt_pk_bf16_f32 v67, v78, v79
	v_cvt_pk_bf16_f32 v66, v74, v75
	ds_read_b128 v[78:81], v150 offset:54272
	v_mfma_f32_32x32x16_bf16 v[50:65], v[88:91], v[70:73], v[50:65]
	v_mul_f32_e32 v2, v2, v76
	v_mul_f32_e32 v3, v3, v76
	v_mul_f32_e32 v20, v20, v104
	v_mul_f32_e32 v21, v21, v104
	v_cvt_pk_bf16_f32 v85, v8, v9
	v_cvt_pk_bf16_f32 v82, v2, v3
	v_pk_mul_f32 v[2:3], v[22:23], v[104:105] op_sel_hi:[1,0]
	v_pk_mul_f32 v[8:9], v[24:25], v[104:105] op_sel_hi:[1,0]
	v_pk_mul_f32 v[18:19], v[18:19], v[104:105] op_sel_hi:[1,0]
	v_mfma_f32_32x32x16_bf16 v[34:49], v[88:91], v[66:69], v[34:49]
	v_cvt_pk_bf16_f32 v84, v102, v103
	v_cvt_pk_bf16_f32 v83, v100, v101
	ds_read_b128 v[86:89], v150 offset:55296
	v_cvt_pk_bf16_f32 v99, v8, v9
	v_cvt_pk_bf16_f32 v98, v2, v3
	v_cvt_pk_bf16_f32 v97, v20, v21
	v_cvt_pk_bf16_f32 v96, v18, v19
	s_waitcnt lgkmcnt(1)
	v_mfma_f32_32x32x16_bf16 v[50:65], v[78:81], v[82:85], v[50:65]
	v_mul_f32_e32 v2, v14, v76
	v_mul_f32_e32 v3, v15, v76
	v_mul_f32_e32 v8, v16, v76
	v_mul_f32_e32 v9, v17, v76
	v_mul_f32_e32 v14, v26, v104
	v_mul_f32_e32 v15, v27, v104
	v_cvt_pk_bf16_f32 v77, v8, v9
	v_cvt_pk_bf16_f32 v76, v2, v3
	v_cvt_pk_bf16_f32 v74, v10, v11
	v_pk_mul_f32 v[2:3], v[28:29], v[104:105] op_sel_hi:[1,0]
	v_mfma_f32_32x32x16_bf16 v[34:49], v[78:81], v[96:99], v[34:49]
	v_mul_f32_e32 v8, v30, v104
	v_mul_f32_e32 v9, v31, v104
	v_mul_f32_e32 v10, v32, v104
	v_mul_f32_e32 v11, v33, v104
	v_cvt_pk_bf16_f32 v75, v12, v13
	v_cvt_pk_bf16_f32 v81, v10, v11
	v_cvt_pk_bf16_f32 v80, v8, v9
	v_cvt_pk_bf16_f32 v79, v2, v3
	v_cvt_pk_bf16_f32 v78, v14, v15
	s_waitcnt lgkmcnt(0)
	v_mfma_f32_32x32x16_bf16 v[50:65], v[86:89], v[74:77], v[50:65]
	v_mfma_f32_32x32x16_bf16 v[34:49], v[86:89], v[78:81], v[34:49]
	ds_read_b128 v[86:89], v150 offset:56320
	ds_read_b128 v[18:21], v150 offset:44032
	ds_read_b128 v[22:25], v150 offset:45056
	ds_read_b128 v[26:29], v150 offset:46080
	ds_read_b128 v[30:33], v150 offset:47104
	ds_read_b128 v[100:103], v150 offset:57344
	s_waitcnt lgkmcnt(1)
	v_mfma_f32_32x32x16_bf16 v[18:33], v[86:89], v[4:7], v[18:33]
	ds_read_b128 v[2:5], v150 offset:48128
	ds_read_b128 v[6:9], v150 offset:49152
	ds_read_b128 v[10:13], v150 offset:50176
	ds_read_b128 v[14:17], v150 offset:51200
	s_waitcnt lgkmcnt(0)
	v_mfma_f32_32x32x16_bf16 v[2:17], v[86:89], v[92:95], v[2:17]
	v_mfma_f32_32x32x16_bf16 v[18:33], v[100:103], v[70:73], v[18:33]
	v_mfma_f32_32x32x16_bf16 v[2:17], v[100:103], v[66:69], v[2:17]
	ds_read_b128 v[66:69], v150 offset:58368
	ds_read_b128 v[70:73], v150 offset:59392
	s_waitcnt lgkmcnt(1)
	v_mfma_f32_32x32x16_bf16 v[18:33], v[66:69], v[82:85], v[18:33]
	v_mfma_f32_32x32x16_bf16 v[2:17], v[66:69], v[96:99], v[2:17]
	s_waitcnt lgkmcnt(0)
	v_mfma_f32_32x32x16_bf16 v[18:33], v[70:73], v[74:77], v[18:33]
	v_mfma_f32_32x32x16_bf16 v[2:17], v[70:73], v[78:81], v[2:17]
	s_nop 10
	v_mul_f32_e32 v66, v22, v22
	v_mul_f32_e32 v67, v23, v23
	v_mul_f32_e32 v68, v30, v30
	v_mul_f32_e32 v69, v31, v31
	v_mul_f32_e32 v70, v24, v24
	v_mul_f32_e32 v71, v25, v25
	v_pk_mul_f32 v[72:73], v[32:33], v[32:33]
	v_pk_mul_f32 v[74:75], v[20:21], v[20:21]
	v_pk_mul_f32 v[76:77], v[28:29], v[28:29]
	v_pk_mul_f32 v[78:79], v[26:27], v[26:27]
	v_pk_mul_f32 v[80:81], v[18:19], v[18:19]
	v_pk_fma_f32 v[78:79], v[58:59], v[58:59], v[78:79]
	v_pk_fma_f32 v[76:77], v[60:61], v[60:61], v[76:77]
	v_pk_fma_f32 v[74:75], v[52:53], v[52:53], v[74:75]
	v_pk_fma_f32 v[72:73], v[64:65], v[64:65], v[72:73]
	v_pk_fma_f32 v[70:71], v[56:57], v[56:57], v[70:71]
	v_pk_fma_f32 v[68:69], v[62:63], v[62:63], v[68:69]
	v_pk_fma_f32 v[66:67], v[54:55], v[54:55], v[66:67]
	v_pk_fma_f32 v[80:81], v[50:51], v[50:51], v[80:81]
	v_pk_add_f32 v[66:67], v[66:67], v[68:69]
	v_pk_add_f32 v[68:69], v[70:71], v[72:73]
	v_pk_add_f32 v[70:71], v[74:75], v[76:77]
	v_pk_add_f32 v[72:73], v[80:81], v[78:79]
	v_pk_add_f32 v[68:69], v[70:71], v[68:69]
	v_pk_add_f32 v[66:67], v[72:73], v[66:67]
	v_pk_mul_f32 v[72:73], v[14:15], v[14:15]
	v_pk_mov_b32 v[70:71], v[66:67], v[68:69] op_sel:[1,0]
	v_mov_b32_e32 v67, v69
	v_pk_add_f32 v[66:67], v[70:71], v[66:67]
	v_pk_mul_f32 v[70:71], v[6:7], v[6:7]
	v_pk_mul_f32 v[74:75], v[8:9], v[8:9]
	v_pk_mul_f32 v[76:77], v[16:17], v[16:17]
	v_pk_mul_f32 v[78:79], v[4:5], v[4:5]
	v_pk_mul_f32 v[80:81], v[12:13], v[12:13]
	v_pk_mul_f32 v[82:83], v[10:11], v[10:11]
	v_pk_mul_f32 v[84:85], v[2:3], v[2:3]
	v_pk_fma_f32 v[82:83], v[42:43], v[42:43], v[82:83]
	v_pk_fma_f32 v[80:81], v[44:45], v[44:45], v[80:81]
	v_pk_fma_f32 v[78:79], v[36:37], v[36:37], v[78:79]
	v_pk_fma_f32 v[76:77], v[48:49], v[48:49], v[76:77]
	v_pk_fma_f32 v[74:75], v[40:41], v[40:41], v[74:75]
	v_pk_fma_f32 v[72:73], v[46:47], v[46:47], v[72:73]
	v_pk_fma_f32 v[70:71], v[38:39], v[38:39], v[70:71]
	v_pk_fma_f32 v[84:85], v[34:35], v[34:35], v[84:85]
	v_pk_add_f32 v[70:71], v[70:71], v[72:73]
	v_pk_add_f32 v[72:73], v[74:75], v[76:77]
	v_pk_add_f32 v[74:75], v[78:79], v[80:81]
	v_pk_add_f32 v[76:77], v[84:85], v[82:83]
	v_pk_add_f32 v[72:73], v[74:75], v[72:73]
	v_pk_add_f32 v[70:71], v[76:77], v[70:71]
	v_pk_add_f32 v[66:67], v[66:67], v[66:67] op_sel:[0,1] op_sel_hi:[1,0]
	v_pk_mov_b32 v[74:75], v[70:71], v[72:73] op_sel:[1,0]
	v_mov_b32_e32 v71, v73
	v_pk_add_f32 v[70:71], v[74:75], v[70:71]
	v_mov_b32_e32 v69, v66
	v_pk_add_f32 v[70:71], v[70:71], v[70:71] op_sel:[0,1] op_sel_hi:[1,0]
	s_nop 0
	v_permlane32_swap_b32_e32 v66, v69
	v_mov_b32_e32 v68, v70
	s_nop 1
	v_permlane32_swap_b32_e32 v70, v68
	v_mov_b32_e32 v71, v66
	v_pk_add_f32 v[66:67], v[70:71], v[68:69]
	v_pk_fma_f32 v[66:67], v[66:67], s[0:1], v[152:153] op_sel_hi:[1,0,0]
	s_mov_b32 s1, 0x800000
	v_mul_f32_e32 v68, 0x4b800000, v67
	v_cmp_gt_f32_e32 vcc, s1, v67
	s_nop 1
	v_cndmask_b32_e32 v67, v67, v68, vcc
	v_rsq_f32_e32 v67, v67
	s_nop 0
	v_mul_f32_e32 v68, 0x45800000, v67
	v_cndmask_b32_e32 v68, v67, v68, vcc
	v_pk_mul_f32 v[158:159], v[50:51], v[68:69] op_sel_hi:[1,0]
	v_pk_mul_f32 v[50:51], v[18:19], v[68:69] op_sel_hi:[1,0]
	v_mul_f32_e32 v18, 0x4b800000, v66
	v_cmp_gt_f32_e32 vcc, s1, v66
	v_pk_mul_f32 v[80:81], v[60:61], v[68:69] op_sel_hi:[1,0]
	v_pk_mul_f32 v[60:61], v[28:29], v[68:69] op_sel_hi:[1,0]
	v_cndmask_b32_e32 v18, v66, v18, vcc
	v_rsq_f32_e32 v18, v18
	v_pk_mul_f32 v[78:79], v[58:59], v[68:69] op_sel_hi:[1,0]
	v_pk_mul_f32 v[160:161], v[52:53], v[68:69] op_sel_hi:[1,0]
	v_pk_mul_f32 v[82:83], v[54:55], v[68:69] op_sel_hi:[1,0]
	v_mul_f32_e32 v19, 0x45800000, v18
	v_cndmask_b32_e32 v28, v18, v19, vcc
	v_pk_mul_f32 v[168:169], v[56:57], v[68:69] op_sel_hi:[1,0]
	v_pk_mul_f32 v[58:59], v[26:27], v[68:69] op_sel_hi:[1,0]
	v_pk_mul_f32 v[52:53], v[20:21], v[68:69] op_sel_hi:[1,0]
	v_pk_mul_f32 v[54:55], v[22:23], v[68:69] op_sel_hi:[1,0]
	v_pk_mul_f32 v[56:57], v[24:25], v[68:69] op_sel_hi:[1,0]
	v_pk_mul_f32 v[18:19], v[42:43], v[28:29] op_sel_hi:[1,0]
	v_pk_mul_f32 v[20:21], v[44:45], v[28:29] op_sel_hi:[1,0]
	v_pk_mul_f32 v[22:23], v[46:47], v[28:29] op_sel_hi:[1,0]
	v_pk_mul_f32 v[26:27], v[48:49], v[28:29] op_sel_hi:[1,0]
	v_pk_mul_f32 v[162:163], v[34:35], v[28:29] op_sel_hi:[1,0]
	v_pk_mul_f32 v[164:165], v[36:37], v[28:29] op_sel_hi:[1,0]
	v_pk_mul_f32 v[166:167], v[38:39], v[28:29] op_sel_hi:[1,0]
	v_pk_mul_f32 v[24:25], v[40:41], v[28:29] op_sel_hi:[1,0]
	v_pk_mul_f32 v[104:105], v[2:3], v[28:29] op_sel_hi:[1,0]
	v_pk_mul_f32 v[112:113], v[4:5], v[28:29] op_sel_hi:[1,0]
	ds_read_b128 v[2:5], v150 offset:60416
	ds_read_b128 v[34:37], v174 offset:32768
	ds_read_b128 v[38:41], v174 offset:32800
	ds_read_b128 v[42:45], v174 offset:32832
	ds_read_b128 v[46:49], v174 offset:32864
	v_cvt_pk_bf16_f32 v129, v168, v169
	v_cvt_pk_bf16_f32 v128, v82, v83
	v_cvt_pk_bf16_f32 v127, v160, v161
	v_cvt_pk_bf16_f32 v126, v158, v159
	v_cvt_pk_bf16_f32 v137, v24, v25
	v_cvt_pk_bf16_f32 v136, v166, v167
	v_cvt_pk_bf16_f32 v135, v164, v165
	s_waitcnt lgkmcnt(0)
	v_mfma_f32_32x32x16_bf16 v[86:101], v[2:5], v[126:129], v[34:49]
	v_cvt_pk_bf16_f32 v134, v162, v163
	v_mul_f32_e32 v84, v62, v68
	v_mul_f32_e32 v85, v63, v68
	v_mul_f32_e32 v170, v64, v68
	v_mul_f32_e32 v171, v65, v68
	v_pk_mul_f32 v[62:63], v[30:31], v[68:69] op_sel_hi:[1,0]
	v_pk_mul_f32 v[64:65], v[32:33], v[68:69] op_sel_hi:[1,0]
	v_pk_mul_f32 v[116:117], v[6:7], v[28:29] op_sel_hi:[1,0]
	v_pk_mul_f32 v[154:155], v[8:9], v[28:29] op_sel_hi:[1,0]
	v_mfma_f32_32x32x16_bf16 v[34:49], v[2:5], v[134:137], v[34:49]
	ds_read_b128 v[6:9], v150 offset:61440
	ds_read_b128 v[66:69], v174 offset:32896
	ds_read_b128 v[106:109], v150 offset:64512
	v_cvt_pk_bf16_f32 v125, v170, v171
	v_cvt_pk_bf16_f32 v124, v84, v85
	v_cvt_pk_bf16_f32 v123, v80, v81
	v_cvt_pk_bf16_f32 v122, v78, v79
	v_cvt_pk_bf16_f32 v149, v26, v27
	v_cvt_pk_bf16_f32 v148, v22, v23
	v_cvt_pk_bf16_f32 v147, v20, v21
	v_cvt_pk_bf16_f32 v146, v18, v19
	s_waitcnt lgkmcnt(2)
	v_mfma_f32_32x32x16_bf16 v[86:101], v[6:9], v[122:125], v[86:101]
	v_mul_f32_e32 v102, v10, v28
	v_mul_f32_e32 v103, v11, v28
	v_mul_f32_e32 v110, v12, v28
	v_mul_f32_e32 v111, v13, v28
	v_mul_f32_e32 v114, v14, v28
	v_mul_f32_e32 v115, v15, v28
	v_pk_mul_f32 v[156:157], v[16:17], v[28:29] op_sel_hi:[1,0]
	ds_read_b128 v[176:179], v174 offset:33536
	ds_read_b128 v[180:183], v174 offset:33568
	ds_read_b128 v[184:187], v174 offset:33600
	ds_read_b128 v[28:31], v174 offset:33632
	ds_read_b128 v[188:191], v174 offset:33792
	ds_read_b128 v[192:195], v174 offset:33824
	ds_read_b128 v[196:199], v174 offset:33856
	ds_read_b128 v[200:203], v174 offset:33888
	ds_read_b128 v[204:207], v150 offset:62464
	v_cvt_pk_bf16_f32 v133, v56, v57
	v_mfma_f32_32x32x16_bf16 v[34:49], v[6:9], v[146:149], v[34:49]
	v_cvt_pk_bf16_f32 v132, v54, v55
	v_cvt_pk_bf16_f32 v131, v52, v53
	v_cvt_pk_bf16_f32 v130, v50, v51
	ds_read_b128 v[70:73], v174 offset:33664
	ds_read_b128 v[74:77], v174 offset:33920
	ds_read_b128 v[208:211], v150 offset:63488
	v_cvt_pk_bf16_f32 v145, v154, v155
	v_cvt_pk_bf16_f32 v144, v116, v117
	v_cvt_pk_bf16_f32 v143, v112, v113
	v_cvt_pk_bf16_f32 v142, v104, v105
	s_waitcnt lgkmcnt(3)
	v_mfma_f32_32x32x16_bf16 v[86:101], v[204:207], v[130:133], v[86:101]
	v_cvt_pk_bf16_f32 v121, v64, v65
	v_cvt_pk_bf16_f32 v120, v62, v63
	v_cvt_pk_bf16_f32 v119, v60, v61
	v_cvt_pk_bf16_f32 v118, v58, v59
	v_cvt_pk_bf16_f32 v141, v156, v157
	v_cvt_pk_bf16_f32 v140, v114, v115
	v_cvt_pk_bf16_f32 v139, v110, v111
	v_mfma_f32_32x32x16_bf16 v[34:49], v[204:207], v[142:145], v[34:49]
	v_cvt_pk_bf16_f32 v138, v102, v103
	v_fma_f32 v16, v30, v170, v202
	v_fma_f32 v17, v31, v171, v203
	v_fma_f32 v14, v28, v84, v200
	v_fma_f32 v15, v29, v85, v201
	v_pk_fma_f32 v[12:13], v[186:187], v[80:81], v[198:199]
	v_pk_fma_f32 v[10:11], v[184:185], v[78:79], v[196:197]
	v_pk_fma_f32 v[8:9], v[182:183], v[168:169], v[194:195]
	s_waitcnt lgkmcnt(0)
	v_mfma_f32_32x32x16_bf16 v[86:101], v[208:211], v[118:121], v[86:101]
	v_fma_f32 v6, v180, v82, v192
	v_fma_f32 v7, v181, v83, v193
	ds_read_b128 v[78:81], v174 offset:33760
	ds_read_b128 v[82:85], v174 offset:33248
	v_fma_f32 v4, v178, v160, v190
	v_fma_f32 v5, v179, v161, v191
	v_pk_fma_f32 v[2:3], v[176:177], v[158:159], v[188:189]
	v_pk_fma_f32 v[32:33], v[30:31], v[26:27], v[202:203]
	v_pk_fma_f32 v[30:31], v[28:29], v[22:23], v[200:201]
	v_pk_fma_f32 v[28:29], v[186:187], v[20:21], v[198:199]
	v_pk_fma_f32 v[26:27], v[184:185], v[18:19], v[196:197]
	v_pk_fma_f32 v[24:25], v[182:183], v[24:25], v[194:195]
	v_pk_fma_f32 v[22:23], v[180:181], v[166:167], v[192:193]
	v_pk_fma_f32 v[20:21], v[178:179], v[164:165], v[190:191]
	v_pk_fma_f32 v[18:19], v[176:177], v[162:163], v[188:189]
	ds_read_b128 v[158:161], v174 offset:33696
	ds_read_b128 v[162:165], v174 offset:33728
	ds_read_b128 v[166:169], v174 offset:33952
	ds_read_b128 v[176:179], v174 offset:33984
	ds_read_b128 v[180:183], v174 offset:34016
	ds_read_b128 v[184:187], v212 offset:11264
	v_mfma_f32_32x32x16_bf16 v[34:49], v[208:211], v[138:141], v[34:49]
	v_cvt_pk_bf16_f32 v86, v86, v87
	v_cvt_pk_bf16_f32 v87, v88, v89
	v_cvt_pk_bf16_f32 v88, v90, v91
	v_cvt_pk_bf16_f32 v89, v92, v93
	ds_read_b128 v[90:93], v212 offset:12288
	v_pk_max_i16 v86, v86, 0
	v_pk_max_i16 v87, v87, 0
	v_pk_max_i16 v88, v88, 0
	v_pk_max_i16 v89, v89, 0
	s_nop 1
	s_nop 0
	v_cvt_pk_bf16_f32 v188, v34, v35
	v_cvt_pk_bf16_f32 v189, v36, v37
	v_cvt_pk_bf16_f32 v190, v38, v39
	v_cvt_pk_bf16_f32 v191, v40, v41
	s_waitcnt lgkmcnt(1)
	v_mfma_f32_32x32x16_bf16 v[2:17], v[184:187], v[86:89], v[2:17]
	v_pk_max_i16 v188, v188, 0
	v_pk_max_i16 v189, v189, 0
	v_pk_max_i16 v190, v190, 0
	v_pk_max_i16 v191, v191, 0
	v_cvt_pk_bf16_f32 v94, v94, v95
	v_cvt_pk_bf16_f32 v95, v96, v97
	v_cvt_pk_bf16_f32 v96, v98, v99
	v_cvt_pk_bf16_f32 v97, v100, v101
	v_cvt_pk_bf16_f32 v98, v42, v43
	v_cvt_pk_bf16_f32 v99, v44, v45
	v_mfma_f32_32x32x16_bf16 v[18:33], v[184:187], v[188:191], v[18:33]
	ds_read_b128 v[184:187], v212 offset:19456
	v_cvt_pk_bf16_f32 v100, v46, v47
	v_cvt_pk_bf16_f32 v101, v48, v49
	v_fma_f32 v64, v80, v64, v182
	v_fma_f32 v65, v81, v65, v183
	v_pk_fma_f32 v[62:63], v[78:79], v[62:63], v[180:181]
	v_pk_fma_f32 v[60:61], v[164:165], v[60:61], v[178:179]
	v_pk_fma_f32 v[58:59], v[162:163], v[58:59], v[176:177]
	v_pk_max_i16 v94, v94, 0
	v_pk_max_i16 v95, v95, 0
	v_pk_max_i16 v96, v96, 0
	v_pk_max_i16 v97, v97, 0
	v_pk_max_i16 v98, v98, 0
	v_pk_max_i16 v99, v99, 0
	v_pk_max_i16 v100, v100, 0
	v_pk_max_i16 v101, v101, 0
	v_pk_fma_f32 v[56:57], v[160:161], v[56:57], v[168:169]
	s_waitcnt lgkmcnt(1)
	v_mfma_f32_32x32x16_bf16 v[2:17], v[90:93], v[94:97], v[2:17]
	v_fma_f32 v54, v158, v54, v166
	v_fma_f32 v55, v159, v55, v167
	v_fma_f32 v52, v72, v52, v76
	v_fma_f32 v53, v73, v53, v77
	v_fma_f32 v50, v70, v50, v74
	v_fma_f32 v51, v71, v51, v75
	v_pk_fma_f32 v[48:49], v[80:81], v[156:157], v[182:183]
	v_pk_fma_f32 v[46:47], v[78:79], v[114:115], v[180:181]
	v_pk_fma_f32 v[44:45], v[164:165], v[110:111], v[178:179]
	v_pk_fma_f32 v[42:43], v[162:163], v[102:103], v[176:177]
	v_mfma_f32_32x32x16_bf16 v[18:33], v[90:93], v[98:101], v[18:33]
	ds_read_b128 v[90:93], v212 offset:20480
	v_fma_f32 v40, v160, v154, v168
	v_fma_f32 v41, v161, v155, v169
	v_fma_f32 v38, v158, v116, v166
	v_fma_f32 v39, v159, v117, v167
	v_pk_fma_f32 v[36:37], v[72:73], v[112:113], v[76:77]
	v_pk_fma_f32 v[34:35], v[70:71], v[104:105], v[74:75]
	s_waitcnt lgkmcnt(1)
	v_mfma_f32_32x32x16_bf16 v[50:65], v[184:187], v[86:89], v[50:65]
	ds_read_b128 v[70:73], v174 offset:32928
	ds_read_b128 v[74:77], v174 offset:32960
	ds_read_b128 v[78:81], v174 offset:32992
	ds_read_b128 v[86:89], v174 offset:33024
	ds_read_b128 v[110:113], v212 offset:1024
	v_mfma_f32_32x32x16_bf16 v[34:49], v[184:187], v[188:191], v[34:49]
	s_waitcnt lgkmcnt(5)
	v_mfma_f32_32x32x16_bf16 v[50:65], v[90:93], v[94:97], v[50:65]
	v_mfma_f32_32x32x16_bf16 v[34:49], v[90:93], v[98:101], v[34:49]
	s_waitcnt lgkmcnt(2)
	v_mfma_f32_32x32x16_bf16 v[90:105], v[106:109], v[126:129], v[66:81]
	v_mfma_f32_32x32x16_bf16 v[66:81], v[106:109], v[134:137], v[66:81]
	ds_read_b128 v[106:109], v212 offset:0
	s_waitcnt lgkmcnt(0)
	v_mfma_f32_32x32x16_bf16 v[90:105], v[106:109], v[122:125], v[90:105]
	v_mfma_f32_32x32x16_bf16 v[66:81], v[106:109], v[146:149], v[66:81]
	ds_read_b128 v[106:109], v212 offset:2048
	v_mfma_f32_32x32x16_bf16 v[90:105], v[110:113], v[130:133], v[90:105]
	v_mfma_f32_32x32x16_bf16 v[66:81], v[110:113], v[142:145], v[66:81]
	ds_read_b128 v[110:113], v212 offset:13312
	s_waitcnt lgkmcnt(1)
	v_mfma_f32_32x32x16_bf16 v[90:105], v[106:109], v[118:121], v[90:105]
	v_mfma_f32_32x32x16_bf16 v[66:81], v[106:109], v[138:141], v[66:81]
	s_nop 10
	v_cvt_pk_bf16_f32 v90, v90, v91
	v_cvt_pk_bf16_f32 v91, v92, v93
	v_cvt_pk_bf16_f32 v92, v94, v95
	v_cvt_pk_bf16_f32 v94, v98, v99
	v_cvt_pk_bf16_f32 v95, v100, v101
	ds_read_b128 v[98:101], v212 offset:21504
	v_cvt_pk_bf16_f32 v66, v66, v67
	v_cvt_pk_bf16_f32 v67, v68, v69
	v_cvt_pk_bf16_f32 v68, v70, v71
	v_cvt_pk_bf16_f32 v93, v96, v97
	v_cvt_pk_bf16_f32 v69, v72, v73
	ds_read_b128 v[70:73], v212 offset:14336
	v_pk_max_i16 v90, v90, 0
	v_pk_max_i16 v91, v91, 0
	v_pk_max_i16 v92, v92, 0
	v_pk_max_i16 v93, v93, 0
	v_pk_max_i16 v66, v66, 0
	v_pk_max_i16 v67, v67, 0
	v_pk_max_i16 v68, v68, 0
	v_pk_max_i16 v69, v69, 0
	v_cvt_pk_bf16_f32 v96, v102, v103
	s_waitcnt lgkmcnt(2)
	v_mfma_f32_32x32x16_bf16 v[2:17], v[110:113], v[90:93], v[2:17]
	v_cvt_pk_bf16_f32 v97, v104, v105
	v_cvt_pk_bf16_f32 v74, v74, v75
	v_cvt_pk_bf16_f32 v75, v76, v77
	v_cvt_pk_bf16_f32 v76, v78, v79
	v_cvt_pk_bf16_f32 v77, v80, v81
	v_pk_max_i16 v94, v94, 0
	v_pk_max_i16 v95, v95, 0
	v_pk_max_i16 v96, v96, 0
	v_pk_max_i16 v97, v97, 0
	v_pk_max_i16 v74, v74, 0
	v_pk_max_i16 v75, v75, 0
	v_pk_max_i16 v76, v76, 0
	v_pk_max_i16 v77, v77, 0
	v_mfma_f32_32x32x16_bf16 v[18:33], v[110:113], v[66:69], v[18:33]
	s_waitcnt lgkmcnt(1)
	v_mfma_f32_32x32x16_bf16 v[34:49], v[98:101], v[66:69], v[34:49]
	ds_read_b128 v[66:69], v212 offset:22528
	v_mfma_f32_32x32x16_bf16 v[50:65], v[98:101], v[90:93], v[50:65]
	s_waitcnt lgkmcnt(1)
	v_mfma_f32_32x32x16_bf16 v[2:17], v[70:73], v[94:97], v[2:17]
	v_mfma_f32_32x32x16_bf16 v[18:33], v[70:73], v[74:77], v[18:33]
	ds_read_b128 v[78:81], v212 offset:3072
	s_waitcnt lgkmcnt(1)
	v_mfma_f32_32x32x16_bf16 v[50:65], v[66:69], v[94:97], v[50:65]
	ds_read_b128 v[90:93], v174 offset:33056
	ds_read_b128 v[94:97], v174 offset:33088
	ds_read_b128 v[98:101], v174 offset:33120
	ds_read_b128 v[70:73], v174 offset:33152
	v_mfma_f32_32x32x16_bf16 v[34:49], v[66:69], v[74:77], v[34:49]
	ds_read_b128 v[66:69], v212 offset:4096
	ds_read_b128 v[74:77], v212 offset:5120
	s_waitcnt lgkmcnt(3)
	v_mfma_f32_32x32x16_bf16 v[102:117], v[78:81], v[126:129], v[86:101]
	v_mfma_f32_32x32x16_bf16 v[86:101], v[78:81], v[134:137], v[86:101]
	s_waitcnt lgkmcnt(1)
	v_mfma_f32_32x32x16_bf16 v[86:101], v[66:69], v[146:149], v[86:101]
	v_mfma_f32_32x32x16_bf16 v[102:117], v[66:69], v[122:125], v[102:117]
	ds_read_b128 v[66:69], v212 offset:6144
	s_waitcnt lgkmcnt(1)
	v_mfma_f32_32x32x16_bf16 v[86:101], v[74:77], v[142:145], v[86:101]
	v_mfma_f32_32x32x16_bf16 v[102:117], v[74:77], v[130:133], v[102:117]
	ds_read_b128 v[74:77], v212 offset:15360
	s_waitcnt lgkmcnt(1)
	v_mfma_f32_32x32x16_bf16 v[86:101], v[66:69], v[138:141], v[86:101]
	v_mfma_f32_32x32x16_bf16 v[102:117], v[66:69], v[118:121], v[102:117]
	s_nop 10
	v_cvt_pk_bf16_f32 v78, v86, v87
	v_cvt_pk_bf16_f32 v80, v90, v91
	v_cvt_pk_bf16_f32 v79, v88, v89
	v_cvt_pk_bf16_f32 v81, v92, v93
	ds_read_b128 v[86:89], v212 offset:16384
	ds_read_b128 v[90:93], v212 offset:23552
	v_cvt_pk_bf16_f32 v66, v102, v103
	v_cvt_pk_bf16_f32 v67, v104, v105
	v_cvt_pk_bf16_f32 v68, v106, v107
	v_cvt_pk_bf16_f32 v69, v108, v109
	v_pk_max_i16 v66, v66, 0
	v_pk_max_i16 v67, v67, 0
	v_pk_max_i16 v68, v68, 0
	v_pk_max_i16 v69, v69, 0
	v_pk_max_i16 v78, v78, 0
	v_pk_max_i16 v79, v79, 0
	v_pk_max_i16 v80, v80, 0
	v_pk_max_i16 v81, v81, 0
	v_cvt_pk_bf16_f32 v94, v94, v95
	s_waitcnt lgkmcnt(2)
	v_mfma_f32_32x32x16_bf16 v[18:33], v[74:77], v[78:81], v[18:33]
	v_cvt_pk_bf16_f32 v95, v96, v97
	v_cvt_pk_bf16_f32 v96, v98, v99
	v_cvt_pk_bf16_f32 v97, v100, v101
	v_pk_max_i16 v94, v94, 0
	v_pk_max_i16 v95, v95, 0
	v_pk_max_i16 v96, v96, 0
	v_pk_max_i16 v97, v97, 0
	v_mfma_f32_32x32x16_bf16 v[2:17], v[74:77], v[66:69], v[2:17]
	v_cvt_pk_bf16_f32 v74, v110, v111
	v_cvt_pk_bf16_f32 v75, v112, v113
	v_cvt_pk_bf16_f32 v76, v114, v115
	v_cvt_pk_bf16_f32 v77, v116, v117
	v_pk_max_i16 v74, v74, 0
	v_pk_max_i16 v75, v75, 0
	v_pk_max_i16 v76, v76, 0
	v_pk_max_i16 v77, v77, 0
	s_waitcnt lgkmcnt(0)
	v_mfma_f32_32x32x16_bf16 v[50:65], v[90:93], v[66:69], v[50:65]
	ds_read_b128 v[66:69], v212 offset:24576
	v_mfma_f32_32x32x16_bf16 v[34:49], v[90:93], v[78:81], v[34:49]
	ds_read_b128 v[102:105], v212 offset:7168
	v_mfma_f32_32x32x16_bf16 v[2:17], v[86:89], v[74:77], v[2:17]
	s_waitcnt lgkmcnt(1)
	v_mfma_f32_32x32x16_bf16 v[50:65], v[66:69], v[74:77], v[50:65]
	ds_read_b128 v[74:77], v174 offset:33184
	ds_read_b128 v[78:81], v174 offset:33216
	v_mfma_f32_32x32x16_bf16 v[34:49], v[66:69], v[94:97], v[34:49]
	ds_read_b128 v[66:69], v212 offset:8192
	v_mfma_f32_32x32x16_bf16 v[18:33], v[86:89], v[94:97], v[18:33]
	s_waitcnt lgkmcnt(1)
	v_mfma_f32_32x32x16_bf16 v[86:101], v[102:105], v[126:129], v[70:85]
	v_mfma_f32_32x32x16_bf16 v[70:85], v[102:105], v[134:137], v[70:85]
	ds_read_b128 v[102:105], v212 offset:9216
	v_lshlrev_b32_e32 v135, 2, v1
	v_add_u32_e32 v134, v172, v174
	s_waitcnt lgkmcnt(1)
	v_mfma_f32_32x32x16_bf16 v[86:101], v[66:69], v[122:125], v[86:101]
	v_mfma_f32_32x32x16_bf16 v[70:85], v[66:69], v[146:149], v[70:85]
	ds_read_b128 v[66:69], v212 offset:10240
	s_waitcnt lgkmcnt(1)
	v_mfma_f32_32x32x16_bf16 v[86:101], v[102:105], v[130:133], v[86:101]
	v_mfma_f32_32x32x16_bf16 v[70:85], v[102:105], v[142:145], v[70:85]
	ds_read_b128 v[102:105], v212 offset:17408
	s_waitcnt lgkmcnt(1)
	v_mfma_f32_32x32x16_bf16 v[86:101], v[66:69], v[118:121], v[86:101]
	v_mfma_f32_32x32x16_bf16 v[70:85], v[66:69], v[138:141], v[70:85]
	s_nop 10
	v_cvt_pk_bf16_f32 v68, v90, v91
	v_cvt_pk_bf16_f32 v69, v92, v93
	ds_read_b128 v[90:93], v212 offset:25600
	v_cvt_pk_bf16_f32 v66, v86, v87
	v_cvt_pk_bf16_f32 v67, v88, v89
	v_pk_max_i16 v66, v66, 0
	v_pk_max_i16 v67, v67, 0
	v_pk_max_i16 v68, v68, 0
	v_pk_max_i16 v69, v69, 0
	v_cvt_pk_bf16_f32 v70, v70, v71
	v_cvt_pk_bf16_f32 v71, v72, v73
	s_waitcnt lgkmcnt(1)
	v_mfma_f32_32x32x16_bf16 v[2:17], v[102:105], v[66:69], v[2:17]
	v_cvt_pk_bf16_f32 v72, v74, v75
	v_cvt_pk_bf16_f32 v73, v76, v77
	ds_read_b128 v[74:77], v212 offset:18432
	v_cvt_pk_bf16_f32 v86, v94, v95
	v_cvt_pk_bf16_f32 v87, v96, v97
	v_cvt_pk_bf16_f32 v88, v98, v99
	s_waitcnt lgkmcnt(1)
	v_mfma_f32_32x32x16_bf16 v[50:65], v[90:93], v[66:69], v[50:65]
	ds_read_b128 v[66:69], v212 offset:26624
	v_cvt_pk_bf16_f32 v89, v100, v101
	v_pk_max_i16 v86, v86, 0
	v_pk_max_i16 v87, v87, 0
	v_pk_max_i16 v88, v88, 0
	v_pk_max_i16 v89, v89, 0
	v_pk_max_i16 v70, v70, 0
	v_pk_max_i16 v71, v71, 0
	v_pk_max_i16 v72, v72, 0
	v_pk_max_i16 v73, v73, 0
	v_cvt_pk_bf16_f32 v78, v78, v79
	v_cvt_pk_bf16_f32 v79, v80, v81
	s_waitcnt lgkmcnt(1)
	v_mfma_f32_32x32x16_bf16 v[2:17], v[74:77], v[86:89], v[2:17]
	v_cvt_pk_bf16_f32 v80, v82, v83
	v_cvt_pk_bf16_f32 v81, v84, v85
	v_pk_max_i16 v78, v78, 0
	v_pk_max_i16 v79, v79, 0
	v_pk_max_i16 v80, v80, 0
	v_pk_max_i16 v81, v81, 0
	s_waitcnt lgkmcnt(0)
	v_mfma_f32_32x32x16_bf16 v[50:65], v[66:69], v[86:89], v[50:65]
	v_mfma_f32_32x32x16_bf16 v[34:49], v[90:93], v[70:73], v[34:49]
	s_nop 10
	v_add_f32_e32 v130, v10, v58
	v_add_f32_e32 v131, v11, v59
	v_add_f32_e32 v132, v12, v60
	v_add_f32_e32 v133, v13, v61
	v_add_f32_e32 v138, v4, v52
	v_add_f32_e32 v139, v5, v53
	v_pk_add_f32 v[140:141], v[16:17], v[64:65]
	v_pk_add_f32 v[142:143], v[8:9], v[56:57]
	v_pk_add_f32 v[144:145], v[14:15], v[62:63]
	v_pk_add_f32 v[146:147], v[6:7], v[54:55]
	v_mfma_f32_32x32x16_bf16 v[18:33], v[102:105], v[70:73], v[18:33]
	ds_read2st64_b32 v[70:71], v135 offset0:133 offset1:134
	v_add_f32_e32 v148, v2, v50
	v_add_f32_e32 v149, v3, v51
	v_add_f32_e32 v144, v146, v144
	v_add_f32_e32 v145, v147, v145
	v_pk_add_f32 v[140:141], v[142:143], v[140:141]
	v_pk_add_f32 v[132:133], v[138:139], v[132:133]
	v_pk_add_f32 v[130:131], v[148:149], v[130:131]
	v_pk_add_f32 v[132:133], v[132:133], v[140:141]
	v_pk_add_f32 v[130:131], v[130:131], v[144:145]
	v_mfma_f32_32x32x16_bf16 v[34:49], v[66:69], v[78:81], v[34:49]
	v_pk_mov_b32 v[138:139], v[130:131], v[132:133] op_sel:[1,0]
	v_mov_b32_e32 v131, v133
	s_waitcnt vmcnt(0) lgkmcnt(0)
	v_mul_f32_e32 v66, v175, v70
	v_pk_add_f32 v[130:131], v[138:139], v[130:131]
	ds_write_b32 v173, v66 offset:512
	v_mul_f32_e32 v66, v175, v71
	v_pk_add_f32 v[130:131], v[130:131], v[130:131] op_sel:[0,1] op_sel_hi:[1,0]
	s_waitcnt lgkmcnt(0)
	ds_read_b128 v[102:105], v174 offset:34560
	ds_read_b128 v[98:101], v174 offset:34592
	ds_read_b128 v[110:113], v174 offset:34624
	ds_read_b128 v[106:109], v174 offset:34656
	ds_read_b128 v[114:117], v174 offset:34688
	ds_read_b128 v[122:125], v174 offset:34720
	ds_read_b128 v[118:121], v174 offset:34752
	ds_read_b128 v[126:129], v174 offset:34784
	v_mov_b32_dpp v66, v66 quad_perm:[1,0,3,2] row_mask:0xf bank_mask:0xf bound_ctrl:1
	v_mov_b32_e32 v131, v130
	v_fmac_f32_e32 v66, v175, v71
	s_nop 0
	v_permlane32_swap_b32_e32 v130, v131
	v_add_f32_dpp v66, v66, v66 quad_perm:[2,3,0,1] row_mask:0xf bank_mask:0xf bound_ctrl:1
	v_add_f32_e32 v130, v130, v131
	v_fmamk_f32 v65, v130, 0xbc800000, v65
	v_add_f32_dpp v66, v66, v66 row_half_mirror row_mask:0xf bank_mask:0xf bound_ctrl:1
	v_fmamk_f32 v64, v130, 0xbc800000, v64
	v_fmamk_f32 v63, v130, 0xbc800000, v63
	v_fmamk_f32 v62, v130, 0xbc800000, v62
	v_fmamk_f32 v61, v130, 0xbc800000, v61
	v_fmamk_f32 v60, v130, 0xbc800000, v60
	v_fmamk_f32 v59, v130, 0xbc800000, v59
	v_fmamk_f32 v58, v130, 0xbc800000, v58
	v_fmamk_f32 v57, v130, 0xbc800000, v57
	v_fmamk_f32 v56, v130, 0xbc800000, v56
	v_fmamk_f32 v55, v130, 0xbc800000, v55
	v_fmamk_f32 v54, v130, 0xbc800000, v54
	v_fmamk_f32 v53, v130, 0xbc800000, v53
	v_fmamk_f32 v52, v130, 0xbc800000, v52
	v_fmamk_f32 v51, v130, 0xbc800000, v51
	v_fmac_f32_e32 v50, 0xbc800000, v130
	v_add_f32_dpp v66, v66, v66 row_ror:8 row_mask:0xf bank_mask:0xf bound_ctrl:1
	v_fmamk_f32 v17, v130, 0xbc800000, v17
	v_fmamk_f32 v16, v130, 0xbc800000, v16
	v_fmamk_f32 v15, v130, 0xbc800000, v15
	v_fmamk_f32 v14, v130, 0xbc800000, v14
	v_fmamk_f32 v13, v130, 0xbc800000, v13
	v_fmamk_f32 v12, v130, 0xbc800000, v12
	v_fmamk_f32 v11, v130, 0xbc800000, v11
	v_fmamk_f32 v10, v130, 0xbc800000, v10
	v_fmamk_f32 v9, v130, 0xbc800000, v9
	v_fmamk_f32 v8, v130, 0xbc800000, v8
	v_fmamk_f32 v7, v130, 0xbc800000, v7
	v_fmamk_f32 v6, v130, 0xbc800000, v6
	v_fmamk_f32 v5, v130, 0xbc800000, v5
	v_fmamk_f32 v4, v130, 0xbc800000, v4
	v_fmamk_f32 v3, v130, 0xbc800000, v3
	v_fmac_f32_e32 v2, 0xbc800000, v130
	v_pk_mul_f32 v[130:131], v[54:55], v[54:55]
	v_pk_mul_f32 v[132:133], v[62:63], v[62:63]
	v_pk_mul_f32 v[138:139], v[50:51], v[50:51]
	v_pk_mul_f32 v[140:141], v[58:59], v[58:59]
	v_pk_mul_f32 v[142:143], v[56:57], v[56:57]
	v_pk_mul_f32 v[144:145], v[64:65], v[64:65]
	v_pk_mul_f32 v[146:147], v[52:53], v[52:53]
	v_pk_mul_f32 v[148:149], v[60:61], v[60:61]
	v_mov_b32_e32 v67, v66
	v_pk_fma_f32 v[148:149], v[12:13], v[12:13], v[148:149]
	v_pk_fma_f32 v[146:147], v[4:5], v[4:5], v[146:147]
	v_pk_fma_f32 v[144:145], v[16:17], v[16:17], v[144:145]
	v_pk_fma_f32 v[142:143], v[8:9], v[8:9], v[142:143]
	v_pk_fma_f32 v[140:141], v[10:11], v[10:11], v[140:141]
	v_pk_fma_f32 v[138:139], v[2:3], v[2:3], v[138:139]
	v_pk_fma_f32 v[132:133], v[14:15], v[14:15], v[132:133]
	v_pk_fma_f32 v[130:131], v[6:7], v[6:7], v[130:131]
	v_permlane16_swap_b32_e32 v66, v67
	v_pk_add_f32 v[130:131], v[130:131], v[132:133]
	v_pk_add_f32 v[132:133], v[138:139], v[140:141]
	v_pk_add_f32 v[138:139], v[142:143], v[144:145]
	v_pk_add_f32 v[140:141], v[146:147], v[148:149]
	v_mfma_f32_32x32x16_bf16 v[18:33], v[74:77], v[78:81], v[18:33]
	v_add_f32_e32 v136, v66, v67
	ds_read_b128 v[70:73], v134 offset:512
	ds_read_b128 v[66:69], v134 offset:544
	ds_read_b128 v[78:81], v134 offset:576
	ds_read_b128 v[74:77], v134 offset:608
	ds_read_b128 v[82:85], v134 offset:640
	ds_read_b128 v[90:93], v134 offset:672
	ds_read_b128 v[86:89], v134 offset:704
	ds_read_b128 v[94:97], v134 offset:736
	v_pk_add_f32 v[138:139], v[140:141], v[138:139]
	v_pk_add_f32 v[130:131], v[132:133], v[130:131]
	s_waitcnt lgkmcnt(8)
	v_pk_mul_f32 v[140:141], v[126:127], v[62:63]
	v_pk_mov_b32 v[132:133], v[130:131], v[138:139] op_sel:[1,0]
	v_mov_b32_e32 v131, v139
	v_pk_mul_f32 v[138:139], v[122:123], v[54:55]
	v_pk_mul_f32 v[142:143], v[114:115], v[50:51]
	v_pk_mul_f32 v[144:145], v[118:119], v[58:59]
	v_pk_mul_f32 v[146:147], v[124:125], v[56:57]
	v_pk_mul_f32 v[148:149], v[128:129], v[64:65]
	v_pk_mul_f32 v[154:155], v[116:117], v[52:53]
	v_pk_mul_f32 v[156:157], v[120:121], v[60:61]
	v_pk_fma_f32 v[154:155], v[104:105], v[4:5], v[154:155]
	v_pk_fma_f32 v[156:157], v[112:113], v[12:13], v[156:157]
	v_pk_fma_f32 v[148:149], v[108:109], v[16:17], v[148:149]
	v_pk_fma_f32 v[146:147], v[100:101], v[8:9], v[146:147]
	v_pk_fma_f32 v[144:145], v[110:111], v[10:11], v[144:145]
	v_pk_fma_f32 v[142:143], v[102:103], v[2:3], v[142:143]
	v_pk_fma_f32 v[140:141], v[106:107], v[14:15], v[140:141]
	v_pk_fma_f32 v[138:139], v[98:99], v[6:7], v[138:139]
	v_pk_add_f32 v[130:131], v[132:133], v[130:131]
	v_pk_add_f32 v[138:139], v[138:139], v[140:141]
	v_pk_add_f32 v[140:141], v[142:143], v[144:145]
	v_pk_add_f32 v[142:143], v[146:147], v[148:149]
	v_pk_add_f32 v[144:145], v[154:155], v[156:157]
	v_pk_add_f32 v[132:133], v[130:131], v[130:131] op_sel:[0,1] op_sel_hi:[1,0]
	v_pk_add_f32 v[142:143], v[144:145], v[142:143]
	v_pk_add_f32 v[138:139], v[140:141], v[138:139]
	v_add_f32_e32 v133, v142, v143
	v_add_f32_e32 v130, v138, v139
	s_waitcnt lgkmcnt(2)
	v_pk_mul_f32 v[138:139], v[90:91], v[54:55]
	s_waitcnt lgkmcnt(0)
	v_pk_mul_f32 v[140:141], v[94:95], v[62:63]
	v_pk_mul_f32 v[142:143], v[82:83], v[50:51]
	v_pk_mul_f32 v[144:145], v[86:87], v[58:59]
	v_pk_mul_f32 v[146:147], v[92:93], v[56:57]
	v_pk_mul_f32 v[148:149], v[96:97], v[64:65]
	v_pk_mul_f32 v[154:155], v[84:85], v[52:53]
	v_pk_mul_f32 v[156:157], v[88:89], v[60:61]
	v_add_f32_e32 v130, v130, v133
	v_pk_fma_f32 v[156:157], v[80:81], v[12:13], v[156:157]
	v_pk_fma_f32 v[154:155], v[72:73], v[4:5], v[154:155]
	v_pk_fma_f32 v[148:149], v[76:77], v[16:17], v[148:149]
	v_pk_fma_f32 v[146:147], v[68:69], v[8:9], v[146:147]
	v_pk_fma_f32 v[144:145], v[78:79], v[10:11], v[144:145]
	v_pk_fma_f32 v[142:143], v[70:71], v[2:3], v[142:143]
	v_pk_fma_f32 v[140:141], v[74:75], v[14:15], v[140:141]
	v_pk_fma_f32 v[138:139], v[66:67], v[6:7], v[138:139]
	v_mov_b32_e32 v133, v130
	v_pk_add_f32 v[138:139], v[138:139], v[140:141]
	v_pk_add_f32 v[140:141], v[142:143], v[144:145]
	v_pk_add_f32 v[142:143], v[146:147], v[148:149]
	v_pk_add_f32 v[144:145], v[154:155], v[156:157]
	v_permlane32_swap_b32_e32 v130, v133
	v_pk_add_f32 v[142:143], v[144:145], v[142:143]
	v_add_f32_e32 v160, v130, v133
	v_pk_add_f32 v[138:139], v[140:141], v[138:139]
	v_add_f32_e32 v133, v142, v143
	v_pk_add_f32 v[140:141], v[26:27], v[42:43]
	v_pk_add_f32 v[142:143], v[28:29], v[44:45]
	v_pk_add_f32 v[144:145], v[20:21], v[36:37]
	v_pk_add_f32 v[146:147], v[32:33], v[48:49]
	v_pk_add_f32 v[148:149], v[24:25], v[40:41]
	v_pk_add_f32 v[154:155], v[30:31], v[46:47]
	v_pk_add_f32 v[156:157], v[22:23], v[38:39]
	v_pk_add_f32 v[158:159], v[18:19], v[34:35]
	v_pk_add_f32 v[154:155], v[156:157], v[154:155]
	v_pk_add_f32 v[146:147], v[148:149], v[146:147]
	v_pk_add_f32 v[142:143], v[144:145], v[142:143]
	v_pk_add_f32 v[140:141], v[158:159], v[140:141]
	v_pk_add_f32 v[142:143], v[142:143], v[146:147]
	v_pk_add_f32 v[140:141], v[140:141], v[154:155]
	v_add_f32_e32 v130, v138, v139
	v_pk_mov_b32 v[144:145], v[140:141], v[142:143] op_sel:[1,0]
	v_mov_b32_e32 v141, v143
	v_pk_add_f32 v[140:141], v[144:145], v[140:141]
	v_add_f32_e32 v133, v130, v133
	v_pk_add_f32 v[140:141], v[140:141], v[140:141] op_sel:[0,1] op_sel_hi:[1,0]
	v_mov_b32_e32 v131, v132
	v_mov_b32_e32 v130, v140
	s_nop 1
	v_permlane32_swap_b32_e32 v140, v130
	v_add_f32_e32 v130, v140, v130
	v_fmamk_f32 v49, v130, 0xbc800000, v49
	v_fmamk_f32 v48, v130, 0xbc800000, v48
	v_fmamk_f32 v47, v130, 0xbc800000, v47
	v_fmamk_f32 v46, v130, 0xbc800000, v46
	v_fmamk_f32 v45, v130, 0xbc800000, v45
	v_fmamk_f32 v44, v130, 0xbc800000, v44
	v_fmamk_f32 v43, v130, 0xbc800000, v43
	v_fmamk_f32 v42, v130, 0xbc800000, v42
	v_fmamk_f32 v41, v130, 0xbc800000, v41
	v_fmamk_f32 v40, v130, 0xbc800000, v40
	v_fmamk_f32 v39, v130, 0xbc800000, v39
	v_fmamk_f32 v38, v130, 0xbc800000, v38
	v_fmamk_f32 v37, v130, 0xbc800000, v37
	v_fmamk_f32 v36, v130, 0xbc800000, v36
	v_fmamk_f32 v35, v130, 0xbc800000, v35
	v_fmac_f32_e32 v34, 0xbc800000, v130
	v_fmamk_f32 v33, v130, 0xbc800000, v33
	v_fmamk_f32 v32, v130, 0xbc800000, v32
	v_fmamk_f32 v31, v130, 0xbc800000, v31
	v_fmamk_f32 v30, v130, 0xbc800000, v30
	v_fmamk_f32 v29, v130, 0xbc800000, v29
	v_fmamk_f32 v28, v130, 0xbc800000, v28
	v_fmamk_f32 v27, v130, 0xbc800000, v27
	v_fmamk_f32 v26, v130, 0xbc800000, v26
	v_fmamk_f32 v25, v130, 0xbc800000, v25
	v_fmamk_f32 v24, v130, 0xbc800000, v24
	v_fmamk_f32 v23, v130, 0xbc800000, v23
	v_fmamk_f32 v22, v130, 0xbc800000, v22
	v_fmamk_f32 v21, v130, 0xbc800000, v21
	v_fmamk_f32 v20, v130, 0xbc800000, v20
	v_fmamk_f32 v19, v130, 0xbc800000, v19
	v_fmac_f32_e32 v18, 0xbc800000, v130
	v_pk_mul_f32 v[140:141], v[38:39], v[38:39]
	v_pk_mul_f32 v[142:143], v[46:47], v[46:47]
	v_pk_mul_f32 v[144:145], v[34:35], v[34:35]
	v_pk_mul_f32 v[146:147], v[42:43], v[42:43]
	v_pk_mul_f32 v[148:149], v[40:41], v[40:41]
	v_pk_mul_f32 v[154:155], v[48:49], v[48:49]
	v_pk_mul_f32 v[156:157], v[36:37], v[36:37]
	v_pk_mul_f32 v[158:159], v[44:45], v[44:45]
	v_pk_fma_f32 v[156:157], v[20:21], v[20:21], v[156:157]
	v_pk_fma_f32 v[158:159], v[28:29], v[28:29], v[158:159]
	v_pk_fma_f32 v[154:155], v[32:33], v[32:33], v[154:155]
	v_pk_fma_f32 v[148:149], v[24:25], v[24:25], v[148:149]
	v_pk_fma_f32 v[146:147], v[26:27], v[26:27], v[146:147]
	v_pk_fma_f32 v[144:145], v[18:19], v[18:19], v[144:145]
	v_pk_fma_f32 v[142:143], v[30:31], v[30:31], v[142:143]
	v_pk_fma_f32 v[140:141], v[22:23], v[22:23], v[140:141]
	v_permlane32_swap_b32_e32 v132, v131
	v_pk_add_f32 v[140:141], v[140:141], v[142:143]
	v_pk_add_f32 v[142:143], v[144:145], v[146:147]
	v_pk_add_f32 v[144:145], v[148:149], v[154:155]
	v_pk_add_f32 v[146:147], v[156:157], v[158:159]
	v_pk_add_f32 v[140:141], v[142:143], v[140:141]
	v_pk_add_f32 v[144:145], v[146:147], v[144:145]
	v_pk_mul_f32 v[122:123], v[122:123], v[38:39]
	v_pk_mov_b32 v[142:143], v[140:141], v[144:145] op_sel:[1,0]
	v_mov_b32_e32 v141, v145
	v_pk_add_f32 v[140:141], v[142:143], v[140:141]
	v_pk_mul_f32 v[126:127], v[126:127], v[46:47]
	v_pk_add_f32 v[140:141], v[140:141], v[140:141] op_sel:[0,1] op_sel_hi:[1,0]
	v_pk_mul_f32 v[114:115], v[114:115], v[34:35]
	v_mov_b32_e32 v130, v140
	s_nop 1
	v_permlane32_swap_b32_e32 v140, v130
	v_mov_b32_e32 v141, v132
	v_pk_add_f32 v[130:131], v[140:141], v[130:131]
	v_pk_mul_f32 v[118:119], v[118:119], v[42:43]
	v_pk_fma_f32 v[130:131], v[130:131], s[0:1], v[152:153] op_sel_hi:[1,0,0]
	v_pk_mul_f32 v[124:125], v[124:125], v[40:41]
	v_mul_f32_e32 v132, 0x4b800000, v131
	v_cmp_gt_f32_e32 vcc, s1, v131
	v_pk_mul_f32 v[128:129], v[128:129], v[48:49]
	v_pk_mul_f32 v[116:117], v[116:117], v[36:37]
	v_pk_mul_f32 v[120:121], v[120:121], v[44:45]
	v_cndmask_b32_e32 v131, v131, v132, vcc
	v_mul_f32_e32 v132, 0x4b800000, v130
	v_cmp_gt_f32_e64 s[0:1], s1, v130
	v_pk_fma_f32 v[112:113], v[112:113], v[28:29], v[120:121]
	v_pk_fma_f32 v[104:105], v[104:105], v[20:21], v[116:117]
	v_pk_fma_f32 v[108:109], v[108:109], v[32:33], v[128:129]
	v_pk_fma_f32 v[100:101], v[100:101], v[24:25], v[124:125]
	v_pk_fma_f32 v[110:111], v[110:111], v[26:27], v[118:119]
	v_pk_fma_f32 v[102:103], v[102:103], v[18:19], v[114:115]
	v_pk_fma_f32 v[106:107], v[106:107], v[30:31], v[126:127]
	v_pk_fma_f32 v[98:99], v[98:99], v[22:23], v[122:123]
	v_rsq_f32_e32 v131, v131
	v_cndmask_b32_e64 v130, v130, v132, s[0:1]
	v_pk_add_f32 v[98:99], v[98:99], v[106:107]
	v_pk_add_f32 v[102:103], v[102:103], v[110:111]
	v_pk_add_f32 v[100:101], v[100:101], v[108:109]
	v_pk_add_f32 v[104:105], v[104:105], v[112:113]
	v_rsq_f32_e32 v132, v130
	v_pk_add_f32 v[100:101], v[104:105], v[100:101]
	v_pk_add_f32 v[98:99], v[102:103], v[98:99]
	v_mul_f32_e32 v130, 0x45800000, v131
	v_add_f32_e32 v98, v98, v99
	v_add_f32_e32 v99, v100, v101
	v_add_f32_e32 v98, v98, v99
	v_mov_b32_e32 v99, v98
	v_pk_mul_f32 v[90:91], v[90:91], v[38:39]
	v_pk_mul_f32 v[94:95], v[94:95], v[46:47]
	v_pk_mul_f32 v[82:83], v[82:83], v[34:35]
	v_pk_mul_f32 v[86:87], v[86:87], v[42:43]
	v_cndmask_b32_e32 v130, v131, v130, vcc
	v_mul_f32_e32 v131, 0x45800000, v132
	v_permlane32_swap_b32_e32 v98, v99
	v_pk_fma_f32 v[78:79], v[78:79], v[26:27], v[86:87]
	v_pk_fma_f32 v[70:71], v[70:71], v[18:19], v[82:83]
	v_pk_fma_f32 v[74:75], v[74:75], v[30:31], v[94:95]
	v_pk_fma_f32 v[66:67], v[66:67], v[22:23], v[90:91]
	v_cndmask_b32_e64 v131, v132, v131, s[0:1]
	v_add_f32_e32 v98, v98, v99
	v_pk_add_f32 v[66:67], v[66:67], v[74:75]
	v_pk_add_f32 v[70:71], v[70:71], v[78:79]
	v_mul_f32_e32 v139, v160, v130
	v_mul_f32_e32 v98, v98, v131
	v_pk_add_f32 v[66:67], v[70:71], v[66:67]
	v_cmp_gt_u32_e32 vcc, 32, v1
	v_add_f32_e32 v66, v66, v67
	v_pk_mul_f32 v[92:93], v[92:93], v[40:41]
	v_cndmask_b32_e32 v67, v98, v139, vcc
	v_add_f32_e32 v67, s12, v67
	v_pk_mul_f32 v[96:97], v[96:97], v[48:49]
	v_pk_mul_f32 v[84:85], v[84:85], v[36:37]
	v_pk_mul_f32 v[88:89], v[88:89], v[44:45]
	v_mul_f32_e32 v67, 0xbfb8aa3b, v67
	v_pk_fma_f32 v[80:81], v[80:81], v[28:29], v[88:89]
	v_pk_fma_f32 v[72:73], v[72:73], v[20:21], v[84:85]
	v_pk_fma_f32 v[76:77], v[76:77], v[32:33], v[96:97]
	v_pk_fma_f32 v[68:69], v[68:69], v[24:25], v[92:93]
	v_exp_f32_e32 v70, v67
	v_pk_add_f32 v[68:69], v[68:69], v[76:77]
	v_pk_add_f32 v[72:73], v[72:73], v[80:81]
	v_cmp_lt_i32_e64 s[0:1], 0, v151
	v_pk_add_f32 v[68:69], v[72:73], v[68:69]
	v_mov_b32_e32 v137, v136
	v_add_f32_e32 v67, v68, v69
	v_add_f32_e32 v67, v66, v67
	v_add_f32_e32 v66, 1.0, v70
	v_rcp_f32_e32 v66, v66
	v_mov_b32_e32 v69, 0xff800000
	v_mov_b32_e32 v138, v133
	v_mov_b32_e32 v68, v67
	v_cndmask_b32_e64 v70, v69, v66, s[0:1]
	v_mbcnt_lo_u32_b32 v66, -1, 0
	v_mbcnt_hi_u32_b32 v66, -1, v66
	v_permlane32_swap_b32_e32 v136, v137
	v_permlane32_swap_b32_e32 v133, v138
	v_permlane32_swap_b32_e32 v67, v68
	v_and_b32_e32 v86, 64, v66
	s_mov_b32 s14, 8
	s_mov_b32 s13, 0
	v_mov_b32_e32 v66, 0
	s_waitcnt lgkmcnt(0)
